# i4 + loop-edge edit: GEMM K-loop back-edge scalar updates (counter / pointer bumps and the exit compare) hoisted above the last barrier of the iteration
# speedup vs baseline: 1.0130x; 1.0057x over previous
.LBB0_198:
	s_add_u32 s20, s18, 0xfff80080
	s_addc_u32 s21, s19, -1
	s_add_i32 s49, 0, 0x10000
	s_cmp_eq_u32 s48, 28
	s_cselect_b32 s23, s15, s21
	s_cselect_b32 s22, s14, s20
	v_add_u32_e32 v2, s49, v1
	s_cselect_b32 s21, s17, s46
	s_cselect_b32 s20, s16, s3
	s_add_i32 s60, 0, 0x14000
	ds_read_b128 v[146:149], v2
	ds_read_b128 v[150:153], v2 offset:1024
	ds_read_b128 v[154:157], v2 offset:2048
	ds_read_b128 v[158:161], v2 offset:3072
	v_add_u32_e32 v2, s60, v1
	ds_read_b128 v[162:165], v2
	ds_read_b128 v[166:169], v2 offset:1024
	ds_read_b128 v[170:173], v2 offset:2048
	ds_read_b128 v[174:177], v2 offset:3072
	v_lshl_add_u64 v[194:195], s[18:19], 0, v[144:145]
	s_add_i32 m0, s34, 0xc000
	ds_read_b128 v[178:181], v133
	ds_read_b128 v[182:185], v133 offset:1024
	ds_read_b128 v[186:189], v133 offset:2048
	ds_read_b128 v[190:193], v133 offset:3072
	ds_read_b128 v[204:207], v133 offset:4096
	ds_read_b128 v[208:211], v133 offset:5120
	ds_read_b128 v[212:215], v133 offset:6144
	ds_read_b128 v[226:229], v133 offset:7168
	global_load_lds_dwordx4 v[194:195], off
	v_lshl_add_u64 v[194:195], s[18:19], 0, v[142:143]
	s_add_i32 m0, s34, 0xe000
	s_nop 0
	global_load_lds_dwordx4 v[194:195], off
	s_waitcnt vmcnt(8)
	s_waitcnt lgkmcnt(0)
	s_barrier
	s_setprio 1
	s_waitcnt lgkmcnt(0)
	v_mfma_f32_16x16x32_bf16 v[128:131], v[146:149], v[178:181], v[128:131]
	v_mfma_f32_16x16x32_bf16 v[124:127], v[154:157], v[178:181], v[124:127]
	v_mfma_f32_16x16x32_bf16 v[112:115], v[146:149], v[186:189], v[112:115]
	v_mfma_f32_16x16x32_bf16 v[108:111], v[154:157], v[186:189], v[108:111]
	v_mfma_f32_16x16x32_bf16 v[96:99], v[146:149], v[204:207], v[96:99]
	v_mfma_f32_16x16x32_bf16 v[92:95], v[154:157], v[204:207], v[92:95]
	v_mfma_f32_16x16x32_bf16 v[80:83], v[146:149], v[212:215], v[80:83]
	v_mfma_f32_16x16x32_bf16 v[76:79], v[154:157], v[212:215], v[76:79]
	v_mfma_f32_16x16x32_bf16 v[128:131], v[150:153], v[182:185], v[128:131]
	v_mfma_f32_16x16x32_bf16 v[124:127], v[158:161], v[182:185], v[124:127]
	v_mfma_f32_16x16x32_bf16 v[112:115], v[150:153], v[190:193], v[112:115]
	v_mfma_f32_16x16x32_bf16 v[108:111], v[158:161], v[190:193], v[108:111]
	v_mfma_f32_16x16x32_bf16 v[96:99], v[150:153], v[208:211], v[96:99]
	v_mfma_f32_16x16x32_bf16 v[92:95], v[158:161], v[208:211], v[92:95]
	v_mfma_f32_16x16x32_bf16 v[80:83], v[150:153], v[226:229], v[80:83]
	v_mfma_f32_16x16x32_bf16 v[76:79], v[158:161], v[226:229], v[76:79]
	s_setprio 0
	s_setprio 1
	v_mfma_f32_16x16x32_bf16 v[120:123], v[162:165], v[178:181], v[120:123]
	v_mfma_f32_16x16x32_bf16 v[116:119], v[170:173], v[178:181], v[116:119]
	v_mfma_f32_16x16x32_bf16 v[104:107], v[162:165], v[186:189], v[104:107]
	v_mfma_f32_16x16x32_bf16 v[100:103], v[170:173], v[186:189], v[100:103]
	v_mfma_f32_16x16x32_bf16 v[88:91], v[162:165], v[204:207], v[88:91]
	v_mfma_f32_16x16x32_bf16 v[84:87], v[170:173], v[204:207], v[84:87]
	v_mfma_f32_16x16x32_bf16 v[72:75], v[162:165], v[212:215], v[72:75]
	v_mfma_f32_16x16x32_bf16 v[68:71], v[170:173], v[212:215], v[68:71]
	v_mfma_f32_16x16x32_bf16 v[120:123], v[166:169], v[182:185], v[120:123]
	v_mfma_f32_16x16x32_bf16 v[116:119], v[174:177], v[182:185], v[116:119]
	v_mfma_f32_16x16x32_bf16 v[104:107], v[166:169], v[190:193], v[104:107]
	v_mfma_f32_16x16x32_bf16 v[100:103], v[174:177], v[190:193], v[100:103]
	v_mfma_f32_16x16x32_bf16 v[88:91], v[166:169], v[208:211], v[88:91]
	v_mfma_f32_16x16x32_bf16 v[84:87], v[174:177], v[208:211], v[84:87]
	v_mfma_f32_16x16x32_bf16 v[72:75], v[166:169], v[226:229], v[72:75]
	v_mfma_f32_16x16x32_bf16 v[68:71], v[174:177], v[226:229], v[68:71]
	s_setprio 0
	s_barrier
	s_add_i32 s49, s49, s31
	v_lshl_add_u64 v[194:195], s[20:21], 0, v[134:135]
	s_mov_b32 m0, s49
	ds_read_b128 v[178:181], v133 offset:16384
	ds_read_b128 v[182:185], v133 offset:17408
	ds_read_b128 v[186:189], v133 offset:18432
	ds_read_b128 v[190:193], v133 offset:19456
	ds_read_b128 v[204:207], v133 offset:20480
	ds_read_b128 v[208:211], v133 offset:21504
	ds_read_b128 v[212:215], v133 offset:22528
	ds_read_b128 v[226:229], v133 offset:23552
	global_load_lds_dwordx4 v[194:195], off
	s_add_i32 m0, s49, 0x2000
	s_add_u32 s58, s20, 0x80000
	v_lshl_add_u64 v[230:231], s[20:21], 0, v[138:139]
	s_addc_u32 s59, s21, 0
	s_add_i32 s49, s60, s31
	global_load_lds_dwordx4 v[230:231], off
	v_lshl_add_u64 v[232:233], s[58:59], 0, v[134:135]
	s_mov_b32 m0, s49
	v_lshl_add_u64 v[234:235], s[22:23], 0, v[140:141]
	global_load_lds_dwordx4 v[232:233], off
	v_lshl_add_u64 v[232:233], s[58:59], 0, v[138:139]
	s_add_i32 m0, s49, 0x2000
	s_nop 0
	global_load_lds_dwordx4 v[232:233], off
	v_lshl_add_u64 v[232:233], s[22:23], 0, v[136:137]
	s_mov_b32 m0, s34
	s_nop 0
	global_load_lds_dwordx4 v[232:233], off
	s_mov_b32 m0, s35
	s_nop 0
	global_load_lds_dwordx4 v[234:235], off
	s_waitcnt vmcnt(8)
	s_waitcnt lgkmcnt(0)
	s_barrier
	s_setprio 1
	s_waitcnt lgkmcnt(0)
	v_mfma_f32_16x16x32_bf16 v[64:67], v[146:149], v[178:181], v[64:67]
	v_mfma_f32_16x16x32_bf16 v[60:63], v[154:157], v[178:181], v[60:63]
	v_mfma_f32_16x16x32_bf16 v[48:51], v[146:149], v[186:189], v[48:51]
	v_mfma_f32_16x16x32_bf16 v[44:47], v[154:157], v[186:189], v[44:47]
	v_mfma_f32_16x16x32_bf16 v[32:35], v[146:149], v[204:207], v[32:35]
	v_mfma_f32_16x16x32_bf16 v[28:31], v[154:157], v[204:207], v[28:31]
	v_mfma_f32_16x16x32_bf16 v[16:19], v[146:149], v[212:215], v[16:19]
	v_mfma_f32_16x16x32_bf16 v[12:15], v[154:157], v[212:215], v[12:15]
	v_mfma_f32_16x16x32_bf16 v[64:67], v[150:153], v[182:185], v[64:67]
	v_mfma_f32_16x16x32_bf16 v[60:63], v[158:161], v[182:185], v[60:63]
	v_mfma_f32_16x16x32_bf16 v[48:51], v[150:153], v[190:193], v[48:51]
	v_mfma_f32_16x16x32_bf16 v[44:47], v[158:161], v[190:193], v[44:47]
	v_mfma_f32_16x16x32_bf16 v[32:35], v[150:153], v[208:211], v[32:35]
	v_mfma_f32_16x16x32_bf16 v[28:31], v[158:161], v[208:211], v[28:31]
	v_mfma_f32_16x16x32_bf16 v[16:19], v[150:153], v[226:229], v[16:19]
	v_mfma_f32_16x16x32_bf16 v[12:15], v[158:161], v[226:229], v[12:15]
	s_setprio 0
	s_setprio 1
	v_mfma_f32_16x16x32_bf16 v[56:59], v[162:165], v[178:181], v[56:59]
	v_mfma_f32_16x16x32_bf16 v[52:55], v[170:173], v[178:181], v[52:55]
	v_mfma_f32_16x16x32_bf16 v[40:43], v[162:165], v[186:189], v[40:43]
	v_mfma_f32_16x16x32_bf16 v[36:39], v[170:173], v[186:189], v[36:39]
	v_mfma_f32_16x16x32_bf16 v[24:27], v[162:165], v[204:207], v[24:27]
	v_mfma_f32_16x16x32_bf16 v[20:23], v[170:173], v[204:207], v[20:23]
	v_mfma_f32_16x16x32_bf16 v[8:11], v[162:165], v[212:215], v[8:11]
	v_mfma_f32_16x16x32_bf16 v[4:7], v[170:173], v[212:215], v[4:7]
	v_mfma_f32_16x16x32_bf16 v[56:59], v[166:169], v[182:185], v[56:59]
	v_mfma_f32_16x16x32_bf16 v[52:55], v[174:177], v[182:185], v[52:55]
	v_mfma_f32_16x16x32_bf16 v[40:43], v[166:169], v[190:193], v[40:43]
	v_mfma_f32_16x16x32_bf16 v[36:39], v[174:177], v[190:193], v[36:39]
	v_mfma_f32_16x16x32_bf16 v[24:27], v[166:169], v[208:211], v[24:27]
	v_mfma_f32_16x16x32_bf16 v[20:23], v[174:177], v[208:211], v[20:23]
	v_mfma_f32_16x16x32_bf16 v[8:11], v[166:169], v[226:229], v[8:11]
	v_mfma_f32_16x16x32_bf16 v[4:7], v[174:177], v[226:229], v[4:7]
	s_setprio 0
	s_barrier
	s_add_i32 s49, 0, 0x18000
	v_add_u32_e32 v2, s49, v1
	s_add_i32 s58, 0, 0x1c000
	ds_read_b128 v[146:149], v2
	ds_read_b128 v[150:153], v2 offset:1024
	ds_read_b128 v[154:157], v2 offset:2048
	ds_read_b128 v[158:161], v2 offset:3072
	v_add_u32_e32 v2, s58, v1
	ds_read_b128 v[162:165], v2
	ds_read_b128 v[166:169], v2 offset:1024
	ds_read_b128 v[170:173], v2 offset:2048
	ds_read_b128 v[174:177], v2 offset:3072
	s_add_u32 s22, s22, 0x80000
	s_addc_u32 s23, s23, 0
	s_mov_b32 m0, s36
	v_lshl_add_u64 v[236:237], s[22:23], 0, v[136:137]
	ds_read_b128 v[178:181], v133 offset:32768
	ds_read_b128 v[182:185], v133 offset:33792
	ds_read_b128 v[186:189], v133 offset:34816
	ds_read_b128 v[190:193], v133 offset:35840
	ds_read_b128 v[204:207], v133 offset:36864
	ds_read_b128 v[208:211], v133 offset:37888
	ds_read_b128 v[212:215], v133 offset:38912
	ds_read_b128 v[226:229], v133 offset:39936
	global_load_lds_dwordx4 v[236:237], off
	v_lshl_add_u64 v[236:237], s[22:23], 0, v[140:141]
	s_mov_b32 m0, s37
	s_nop 0
	global_load_lds_dwordx4 v[236:237], off
	s_waitcnt vmcnt(8)
	s_waitcnt lgkmcnt(0)
	s_barrier
	s_setprio 1
	s_waitcnt lgkmcnt(0)
	v_mfma_f32_16x16x32_bf16 v[128:131], v[146:149], v[178:181], v[128:131]
	v_mfma_f32_16x16x32_bf16 v[124:127], v[154:157], v[178:181], v[124:127]
	v_mfma_f32_16x16x32_bf16 v[112:115], v[146:149], v[186:189], v[112:115]
	v_mfma_f32_16x16x32_bf16 v[108:111], v[154:157], v[186:189], v[108:111]
	v_mfma_f32_16x16x32_bf16 v[96:99], v[146:149], v[204:207], v[96:99]
	v_mfma_f32_16x16x32_bf16 v[92:95], v[154:157], v[204:207], v[92:95]
	v_mfma_f32_16x16x32_bf16 v[80:83], v[146:149], v[212:215], v[80:83]
	v_mfma_f32_16x16x32_bf16 v[76:79], v[154:157], v[212:215], v[76:79]
	v_mfma_f32_16x16x32_bf16 v[128:131], v[150:153], v[182:185], v[128:131]
	v_mfma_f32_16x16x32_bf16 v[124:127], v[158:161], v[182:185], v[124:127]
	v_mfma_f32_16x16x32_bf16 v[112:115], v[150:153], v[190:193], v[112:115]
	v_mfma_f32_16x16x32_bf16 v[108:111], v[158:161], v[190:193], v[108:111]
	v_mfma_f32_16x16x32_bf16 v[96:99], v[150:153], v[208:211], v[96:99]
	v_mfma_f32_16x16x32_bf16 v[92:95], v[158:161], v[208:211], v[92:95]
	v_mfma_f32_16x16x32_bf16 v[80:83], v[150:153], v[226:229], v[80:83]
	v_mfma_f32_16x16x32_bf16 v[76:79], v[158:161], v[226:229], v[76:79]
	s_setprio 0
	s_setprio 1
	v_mfma_f32_16x16x32_bf16 v[120:123], v[162:165], v[178:181], v[120:123]
	v_mfma_f32_16x16x32_bf16 v[116:119], v[170:173], v[178:181], v[116:119]
	v_mfma_f32_16x16x32_bf16 v[104:107], v[162:165], v[186:189], v[104:107]
	v_mfma_f32_16x16x32_bf16 v[100:103], v[170:173], v[186:189], v[100:103]
	v_mfma_f32_16x16x32_bf16 v[88:91], v[162:165], v[204:207], v[88:91]
	v_mfma_f32_16x16x32_bf16 v[84:87], v[170:173], v[204:207], v[84:87]
	v_mfma_f32_16x16x32_bf16 v[72:75], v[162:165], v[212:215], v[72:75]
	v_mfma_f32_16x16x32_bf16 v[68:71], v[170:173], v[212:215], v[68:71]
	v_mfma_f32_16x16x32_bf16 v[120:123], v[166:169], v[182:185], v[120:123]
	v_mfma_f32_16x16x32_bf16 v[116:119], v[174:177], v[182:185], v[116:119]
	v_mfma_f32_16x16x32_bf16 v[104:107], v[166:169], v[190:193], v[104:107]
	v_mfma_f32_16x16x32_bf16 v[100:103], v[174:177], v[190:193], v[100:103]
	v_mfma_f32_16x16x32_bf16 v[88:91], v[166:169], v[208:211], v[88:91]
	v_mfma_f32_16x16x32_bf16 v[84:87], v[174:177], v[208:211], v[84:87]
	v_mfma_f32_16x16x32_bf16 v[72:75], v[166:169], v[226:229], v[72:75]
	v_mfma_f32_16x16x32_bf16 v[68:71], v[174:177], v[226:229], v[68:71]
	s_setprio 0
	s_barrier
	s_add_i32 s22, s49, s31
	v_lshl_add_u64 v[194:195], v[194:195], 0, s[94:95]
	s_mov_b32 m0, s22
	ds_read_b128 v[178:181], v133 offset:49152
	ds_read_b128 v[182:185], v133 offset:50176
	ds_read_b128 v[186:189], v133 offset:51200
	ds_read_b128 v[190:193], v133 offset:52224
	ds_read_b128 v[204:207], v133 offset:53248
	ds_read_b128 v[208:211], v133 offset:54272
	ds_read_b128 v[212:215], v133 offset:55296
	ds_read_b128 v[226:229], v133 offset:56320
	global_load_lds_dwordx4 v[194:195], off
	s_add_i32 m0, s22, 0x2000
	s_add_u32 s20, s20, 0x80080
	v_lshl_add_u64 v[194:195], v[230:231], 0, s[94:95]
	s_addc_u32 s21, s21, 0
	s_add_i32 s22, s58, s31
	global_load_lds_dwordx4 v[194:195], off
	v_lshl_add_u64 v[194:195], s[20:21], 0, v[134:135]
	s_mov_b32 m0, s22
	s_nop 0
	global_load_lds_dwordx4 v[194:195], off
	v_lshl_add_u64 v[194:195], s[20:21], 0, v[138:139]
	s_add_i32 m0, s22, 0x2000
	s_nop 0
	global_load_lds_dwordx4 v[194:195], off
	v_lshl_add_u64 v[194:195], v[232:233], 0, s[94:95]
	s_mov_b32 m0, s40
	s_nop 0
	global_load_lds_dwordx4 v[194:195], off
	v_lshl_add_u64 v[194:195], v[234:235], 0, s[94:95]
	s_mov_b32 m0, s41
	s_nop 0
	global_load_lds_dwordx4 v[194:195], off
	s_waitcnt vmcnt(8)
	s_waitcnt lgkmcnt(0)
	s_barrier
	s_setprio 1
	s_waitcnt lgkmcnt(0)
	v_mfma_f32_16x16x32_bf16 v[64:67], v[146:149], v[178:181], v[64:67]
	v_mfma_f32_16x16x32_bf16 v[60:63], v[154:157], v[178:181], v[60:63]
	v_mfma_f32_16x16x32_bf16 v[48:51], v[146:149], v[186:189], v[48:51]
	v_mfma_f32_16x16x32_bf16 v[44:47], v[154:157], v[186:189], v[44:47]
	v_mfma_f32_16x16x32_bf16 v[32:35], v[146:149], v[204:207], v[32:35]
	v_mfma_f32_16x16x32_bf16 v[28:31], v[154:157], v[204:207], v[28:31]
	v_mfma_f32_16x16x32_bf16 v[16:19], v[146:149], v[212:215], v[16:19]
	v_mfma_f32_16x16x32_bf16 v[12:15], v[154:157], v[212:215], v[12:15]
	v_mfma_f32_16x16x32_bf16 v[64:67], v[150:153], v[182:185], v[64:67]
	v_mfma_f32_16x16x32_bf16 v[60:63], v[158:161], v[182:185], v[60:63]
	v_mfma_f32_16x16x32_bf16 v[48:51], v[150:153], v[190:193], v[48:51]
	v_mfma_f32_16x16x32_bf16 v[44:47], v[158:161], v[190:193], v[44:47]
	v_mfma_f32_16x16x32_bf16 v[32:35], v[150:153], v[208:211], v[32:35]
	v_mfma_f32_16x16x32_bf16 v[28:31], v[158:161], v[208:211], v[28:31]
	v_mfma_f32_16x16x32_bf16 v[16:19], v[150:153], v[226:229], v[16:19]
	v_mfma_f32_16x16x32_bf16 v[12:15], v[158:161], v[226:229], v[12:15]
	s_setprio 0
	s_setprio 1
	v_mfma_f32_16x16x32_bf16 v[56:59], v[162:165], v[178:181], v[56:59]
	v_mfma_f32_16x16x32_bf16 v[52:55], v[170:173], v[178:181], v[52:55]
	v_mfma_f32_16x16x32_bf16 v[40:43], v[162:165], v[186:189], v[40:43]
	v_mfma_f32_16x16x32_bf16 v[36:39], v[170:173], v[186:189], v[36:39]
	v_mfma_f32_16x16x32_bf16 v[24:27], v[162:165], v[204:207], v[24:27]
	v_mfma_f32_16x16x32_bf16 v[20:23], v[170:173], v[204:207], v[20:23]
	v_mfma_f32_16x16x32_bf16 v[8:11], v[162:165], v[212:215], v[8:11]
	v_mfma_f32_16x16x32_bf16 v[4:7], v[170:173], v[212:215], v[4:7]
	v_mfma_f32_16x16x32_bf16 v[56:59], v[166:169], v[182:185], v[56:59]
	v_mfma_f32_16x16x32_bf16 v[52:55], v[174:177], v[182:185], v[52:55]
	v_mfma_f32_16x16x32_bf16 v[40:43], v[166:169], v[190:193], v[40:43]
	v_mfma_f32_16x16x32_bf16 v[36:39], v[174:177], v[190:193], v[36:39]
	v_mfma_f32_16x16x32_bf16 v[24:27], v[166:169], v[208:211], v[24:27]
	v_mfma_f32_16x16x32_bf16 v[20:23], v[174:177], v[208:211], v[20:23]
	v_mfma_f32_16x16x32_bf16 v[8:11], v[166:169], v[226:229], v[8:11]
	v_mfma_f32_16x16x32_bf16 v[4:7], v[174:177], v[226:229], v[4:7]
	s_setprio 0
	s_add_i32 s48, s48, 2
	s_add_u32 s3, s3, 0x100
	s_addc_u32 s46, s46, 0
	s_add_u32 s18, s18, 0x100
	s_addc_u32 s19, s19, 0
	s_cmp_gt_u32 s48, 29
	s_barrier
	s_cbranch_scc0 .LBB0_198
	s_and_b64 vcc, exec, s[10:11]
	s_cbranch_vccz .LBB0_201
	s_barrier

.LBB0_236:
	s_add_u32 s20, s18, 0xfff80080
	s_addc_u32 s21, s19, -1
	s_add_i32 s58, 0, 0x10000
	s_cmp_eq_u32 s49, 28
	s_cselect_b32 s23, s15, s21
	s_cselect_b32 s22, s14, s20
	v_add_u32_e32 v2, s58, v1
	s_cselect_b32 s21, s17, s46
	s_cselect_b32 s20, s16, s3
	s_add_i32 s60, 0, 0x14000
	ds_read_b128 v[146:149], v2
	ds_read_b128 v[150:153], v2 offset:1024
	ds_read_b128 v[154:157], v2 offset:2048
	ds_read_b128 v[158:161], v2 offset:3072
	v_add_u32_e32 v2, s60, v1
	ds_read_b128 v[162:165], v2
	ds_read_b128 v[166:169], v2 offset:1024
	ds_read_b128 v[170:173], v2 offset:2048
	ds_read_b128 v[174:177], v2 offset:3072
	v_lshl_add_u64 v[194:195], s[18:19], 0, v[144:145]
	s_add_i32 m0, s35, 0xc000
	ds_read_b128 v[178:181], v133
	ds_read_b128 v[182:185], v133 offset:1024
	ds_read_b128 v[186:189], v133 offset:2048
	ds_read_b128 v[190:193], v133 offset:3072
	ds_read_b128 v[204:207], v133 offset:4096
	ds_read_b128 v[208:211], v133 offset:5120
	ds_read_b128 v[212:215], v133 offset:6144
	ds_read_b128 v[226:229], v133 offset:7168
	global_load_lds_dwordx4 v[194:195], off
	v_lshl_add_u64 v[194:195], s[18:19], 0, v[142:143]
	s_add_i32 m0, s35, 0xe000
	s_nop 0
	global_load_lds_dwordx4 v[194:195], off
	s_waitcnt vmcnt(8)
	s_waitcnt lgkmcnt(0)
	s_barrier
	s_setprio 1
	s_waitcnt lgkmcnt(0)
	v_mfma_f32_16x16x32_bf16 v[128:131], v[146:149], v[178:181], v[128:131]
	v_mfma_f32_16x16x32_bf16 v[124:127], v[154:157], v[178:181], v[124:127]
	v_mfma_f32_16x16x32_bf16 v[112:115], v[146:149], v[186:189], v[112:115]
	v_mfma_f32_16x16x32_bf16 v[108:111], v[154:157], v[186:189], v[108:111]
	v_mfma_f32_16x16x32_bf16 v[96:99], v[146:149], v[204:207], v[96:99]
	v_mfma_f32_16x16x32_bf16 v[92:95], v[154:157], v[204:207], v[92:95]
	v_mfma_f32_16x16x32_bf16 v[80:83], v[146:149], v[212:215], v[80:83]
	v_mfma_f32_16x16x32_bf16 v[76:79], v[154:157], v[212:215], v[76:79]
	v_mfma_f32_16x16x32_bf16 v[128:131], v[150:153], v[182:185], v[128:131]
	v_mfma_f32_16x16x32_bf16 v[124:127], v[158:161], v[182:185], v[124:127]
	v_mfma_f32_16x16x32_bf16 v[112:115], v[150:153], v[190:193], v[112:115]
	v_mfma_f32_16x16x32_bf16 v[108:111], v[158:161], v[190:193], v[108:111]
	v_mfma_f32_16x16x32_bf16 v[96:99], v[150:153], v[208:211], v[96:99]
	v_mfma_f32_16x16x32_bf16 v[92:95], v[158:161], v[208:211], v[92:95]
	v_mfma_f32_16x16x32_bf16 v[80:83], v[150:153], v[226:229], v[80:83]
	v_mfma_f32_16x16x32_bf16 v[76:79], v[158:161], v[226:229], v[76:79]
	s_setprio 0
	s_setprio 1
	v_mfma_f32_16x16x32_bf16 v[120:123], v[162:165], v[178:181], v[120:123]
	v_mfma_f32_16x16x32_bf16 v[116:119], v[170:173], v[178:181], v[116:119]
	v_mfma_f32_16x16x32_bf16 v[104:107], v[162:165], v[186:189], v[104:107]
	v_mfma_f32_16x16x32_bf16 v[100:103], v[170:173], v[186:189], v[100:103]
	v_mfma_f32_16x16x32_bf16 v[88:91], v[162:165], v[204:207], v[88:91]
	v_mfma_f32_16x16x32_bf16 v[84:87], v[170:173], v[204:207], v[84:87]
	v_mfma_f32_16x16x32_bf16 v[72:75], v[162:165], v[212:215], v[72:75]
	v_mfma_f32_16x16x32_bf16 v[68:71], v[170:173], v[212:215], v[68:71]
	v_mfma_f32_16x16x32_bf16 v[120:123], v[166:169], v[182:185], v[120:123]
	v_mfma_f32_16x16x32_bf16 v[116:119], v[174:177], v[182:185], v[116:119]
	v_mfma_f32_16x16x32_bf16 v[104:107], v[166:169], v[190:193], v[104:107]
	v_mfma_f32_16x16x32_bf16 v[100:103], v[174:177], v[190:193], v[100:103]
	v_mfma_f32_16x16x32_bf16 v[88:91], v[166:169], v[208:211], v[88:91]
	v_mfma_f32_16x16x32_bf16 v[84:87], v[174:177], v[208:211], v[84:87]
	v_mfma_f32_16x16x32_bf16 v[72:75], v[166:169], v[226:229], v[72:75]
	v_mfma_f32_16x16x32_bf16 v[68:71], v[174:177], v[226:229], v[68:71]
	s_setprio 0
	s_barrier
	s_add_i32 s58, s58, s34
	v_lshl_add_u64 v[194:195], s[20:21], 0, v[134:135]
	s_mov_b32 m0, s58
	ds_read_b128 v[178:181], v133 offset:16384
	ds_read_b128 v[182:185], v133 offset:17408
	ds_read_b128 v[186:189], v133 offset:18432
	ds_read_b128 v[190:193], v133 offset:19456
	ds_read_b128 v[204:207], v133 offset:20480
	ds_read_b128 v[208:211], v133 offset:21504
	ds_read_b128 v[212:215], v133 offset:22528
	ds_read_b128 v[226:229], v133 offset:23552
	global_load_lds_dwordx4 v[194:195], off
	s_add_i32 m0, s58, 0x2000
	s_add_u32 s58, s20, 0x80000
	v_lshl_add_u64 v[230:231], s[20:21], 0, v[138:139]
	s_addc_u32 s59, s21, 0
	s_add_i32 s60, s60, s34
	global_load_lds_dwordx4 v[230:231], off
	v_lshl_add_u64 v[232:233], s[58:59], 0, v[134:135]
	s_mov_b32 m0, s60
	v_lshl_add_u64 v[234:235], s[22:23], 0, v[140:141]
	global_load_lds_dwordx4 v[232:233], off
	v_lshl_add_u64 v[232:233], s[58:59], 0, v[138:139]
	s_add_i32 m0, s60, 0x2000
	s_nop 0
	global_load_lds_dwordx4 v[232:233], off
	v_lshl_add_u64 v[232:233], s[22:23], 0, v[136:137]
	s_mov_b32 m0, s35
	s_nop 0
	global_load_lds_dwordx4 v[232:233], off
	s_mov_b32 m0, s36
	s_nop 0
	global_load_lds_dwordx4 v[234:235], off
	s_waitcnt vmcnt(8)
	s_waitcnt lgkmcnt(0)
	s_barrier
	s_setprio 1
	s_waitcnt lgkmcnt(0)
	v_mfma_f32_16x16x32_bf16 v[64:67], v[146:149], v[178:181], v[64:67]
	v_mfma_f32_16x16x32_bf16 v[60:63], v[154:157], v[178:181], v[60:63]
	v_mfma_f32_16x16x32_bf16 v[48:51], v[146:149], v[186:189], v[48:51]
	v_mfma_f32_16x16x32_bf16 v[44:47], v[154:157], v[186:189], v[44:47]
	v_mfma_f32_16x16x32_bf16 v[32:35], v[146:149], v[204:207], v[32:35]
	v_mfma_f32_16x16x32_bf16 v[28:31], v[154:157], v[204:207], v[28:31]
	v_mfma_f32_16x16x32_bf16 v[16:19], v[146:149], v[212:215], v[16:19]
	v_mfma_f32_16x16x32_bf16 v[12:15], v[154:157], v[212:215], v[12:15]
	v_mfma_f32_16x16x32_bf16 v[64:67], v[150:153], v[182:185], v[64:67]
	v_mfma_f32_16x16x32_bf16 v[60:63], v[158:161], v[182:185], v[60:63]
	v_mfma_f32_16x16x32_bf16 v[48:51], v[150:153], v[190:193], v[48:51]
	v_mfma_f32_16x16x32_bf16 v[44:47], v[158:161], v[190:193], v[44:47]
	v_mfma_f32_16x16x32_bf16 v[32:35], v[150:153], v[208:211], v[32:35]
	v_mfma_f32_16x16x32_bf16 v[28:31], v[158:161], v[208:211], v[28:31]
	v_mfma_f32_16x16x32_bf16 v[16:19], v[150:153], v[226:229], v[16:19]
	v_mfma_f32_16x16x32_bf16 v[12:15], v[158:161], v[226:229], v[12:15]
	s_setprio 0
	s_setprio 1
	v_mfma_f32_16x16x32_bf16 v[56:59], v[162:165], v[178:181], v[56:59]
	v_mfma_f32_16x16x32_bf16 v[52:55], v[170:173], v[178:181], v[52:55]
	v_mfma_f32_16x16x32_bf16 v[40:43], v[162:165], v[186:189], v[40:43]
	v_mfma_f32_16x16x32_bf16 v[36:39], v[170:173], v[186:189], v[36:39]
	v_mfma_f32_16x16x32_bf16 v[24:27], v[162:165], v[204:207], v[24:27]
	v_mfma_f32_16x16x32_bf16 v[20:23], v[170:173], v[204:207], v[20:23]
	v_mfma_f32_16x16x32_bf16 v[8:11], v[162:165], v[212:215], v[8:11]
	v_mfma_f32_16x16x32_bf16 v[4:7], v[170:173], v[212:215], v[4:7]
	v_mfma_f32_16x16x32_bf16 v[56:59], v[166:169], v[182:185], v[56:59]
	v_mfma_f32_16x16x32_bf16 v[52:55], v[174:177], v[182:185], v[52:55]
	v_mfma_f32_16x16x32_bf16 v[40:43], v[166:169], v[190:193], v[40:43]
	v_mfma_f32_16x16x32_bf16 v[36:39], v[174:177], v[190:193], v[36:39]
	v_mfma_f32_16x16x32_bf16 v[24:27], v[166:169], v[208:211], v[24:27]
	v_mfma_f32_16x16x32_bf16 v[20:23], v[174:177], v[208:211], v[20:23]
	v_mfma_f32_16x16x32_bf16 v[8:11], v[166:169], v[226:229], v[8:11]
	v_mfma_f32_16x16x32_bf16 v[4:7], v[174:177], v[226:229], v[4:7]
	s_setprio 0
	s_barrier
	s_add_i32 s58, 0, 0x18000
	v_add_u32_e32 v2, s58, v1
	s_add_i32 s59, 0, 0x1c000
	ds_read_b128 v[146:149], v2
	ds_read_b128 v[150:153], v2 offset:1024
	ds_read_b128 v[154:157], v2 offset:2048
	ds_read_b128 v[158:161], v2 offset:3072
	v_add_u32_e32 v2, s59, v1
	ds_read_b128 v[162:165], v2
	ds_read_b128 v[166:169], v2 offset:1024
	ds_read_b128 v[170:173], v2 offset:2048
	ds_read_b128 v[174:177], v2 offset:3072
	s_add_u32 s22, s22, 0x80000
	s_addc_u32 s23, s23, 0
	s_mov_b32 m0, s37
	v_lshl_add_u64 v[236:237], s[22:23], 0, v[136:137]
	ds_read_b128 v[178:181], v133 offset:32768
	ds_read_b128 v[182:185], v133 offset:33792
	ds_read_b128 v[186:189], v133 offset:34816
	ds_read_b128 v[190:193], v133 offset:35840
	ds_read_b128 v[204:207], v133 offset:36864
	ds_read_b128 v[208:211], v133 offset:37888
	ds_read_b128 v[212:215], v133 offset:38912
	ds_read_b128 v[226:229], v133 offset:39936
	global_load_lds_dwordx4 v[236:237], off
	v_lshl_add_u64 v[236:237], s[22:23], 0, v[140:141]
	s_mov_b32 m0, s38
	s_nop 0
	global_load_lds_dwordx4 v[236:237], off
	s_waitcnt vmcnt(8)
	s_waitcnt lgkmcnt(0)
	s_barrier
	s_setprio 1
	s_waitcnt lgkmcnt(0)
	v_mfma_f32_16x16x32_bf16 v[128:131], v[146:149], v[178:181], v[128:131]
	v_mfma_f32_16x16x32_bf16 v[124:127], v[154:157], v[178:181], v[124:127]
	v_mfma_f32_16x16x32_bf16 v[112:115], v[146:149], v[186:189], v[112:115]
	v_mfma_f32_16x16x32_bf16 v[108:111], v[154:157], v[186:189], v[108:111]
	v_mfma_f32_16x16x32_bf16 v[96:99], v[146:149], v[204:207], v[96:99]
	v_mfma_f32_16x16x32_bf16 v[92:95], v[154:157], v[204:207], v[92:95]
	v_mfma_f32_16x16x32_bf16 v[80:83], v[146:149], v[212:215], v[80:83]
	v_mfma_f32_16x16x32_bf16 v[76:79], v[154:157], v[212:215], v[76:79]
	v_mfma_f32_16x16x32_bf16 v[128:131], v[150:153], v[182:185], v[128:131]
	v_mfma_f32_16x16x32_bf16 v[124:127], v[158:161], v[182:185], v[124:127]
	v_mfma_f32_16x16x32_bf16 v[112:115], v[150:153], v[190:193], v[112:115]
	v_mfma_f32_16x16x32_bf16 v[108:111], v[158:161], v[190:193], v[108:111]
	v_mfma_f32_16x16x32_bf16 v[96:99], v[150:153], v[208:211], v[96:99]
	v_mfma_f32_16x16x32_bf16 v[92:95], v[158:161], v[208:211], v[92:95]
	v_mfma_f32_16x16x32_bf16 v[80:83], v[150:153], v[226:229], v[80:83]
	v_mfma_f32_16x16x32_bf16 v[76:79], v[158:161], v[226:229], v[76:79]
	s_setprio 0
	s_setprio 1
	v_mfma_f32_16x16x32_bf16 v[120:123], v[162:165], v[178:181], v[120:123]
	v_mfma_f32_16x16x32_bf16 v[116:119], v[170:173], v[178:181], v[116:119]
	v_mfma_f32_16x16x32_bf16 v[104:107], v[162:165], v[186:189], v[104:107]
	v_mfma_f32_16x16x32_bf16 v[100:103], v[170:173], v[186:189], v[100:103]
	v_mfma_f32_16x16x32_bf16 v[88:91], v[162:165], v[204:207], v[88:91]
	v_mfma_f32_16x16x32_bf16 v[84:87], v[170:173], v[204:207], v[84:87]
	v_mfma_f32_16x16x32_bf16 v[72:75], v[162:165], v[212:215], v[72:75]
	v_mfma_f32_16x16x32_bf16 v[68:71], v[170:173], v[212:215], v[68:71]
	v_mfma_f32_16x16x32_bf16 v[120:123], v[166:169], v[182:185], v[120:123]
	v_mfma_f32_16x16x32_bf16 v[116:119], v[174:177], v[182:185], v[116:119]
	v_mfma_f32_16x16x32_bf16 v[104:107], v[166:169], v[190:193], v[104:107]
	v_mfma_f32_16x16x32_bf16 v[100:103], v[174:177], v[190:193], v[100:103]
	v_mfma_f32_16x16x32_bf16 v[88:91], v[166:169], v[208:211], v[88:91]
	v_mfma_f32_16x16x32_bf16 v[84:87], v[174:177], v[208:211], v[84:87]
	v_mfma_f32_16x16x32_bf16 v[72:75], v[166:169], v[226:229], v[72:75]
	v_mfma_f32_16x16x32_bf16 v[68:71], v[174:177], v[226:229], v[68:71]
	s_setprio 0
	s_barrier
	s_add_i32 s22, s58, s34
	v_lshl_add_u64 v[194:195], v[194:195], 0, s[94:95]
	s_mov_b32 m0, s22
	ds_read_b128 v[178:181], v133 offset:49152
	ds_read_b128 v[182:185], v133 offset:50176
	ds_read_b128 v[186:189], v133 offset:51200
	ds_read_b128 v[190:193], v133 offset:52224
	ds_read_b128 v[204:207], v133 offset:53248
	ds_read_b128 v[208:211], v133 offset:54272
	ds_read_b128 v[212:215], v133 offset:55296
	ds_read_b128 v[226:229], v133 offset:56320
	global_load_lds_dwordx4 v[194:195], off
	s_add_i32 m0, s22, 0x2000
	s_add_u32 s20, s20, 0x80080
	v_lshl_add_u64 v[194:195], v[230:231], 0, s[94:95]
	s_addc_u32 s21, s21, 0
	s_add_i32 s22, s59, s34
	global_load_lds_dwordx4 v[194:195], off
	v_lshl_add_u64 v[194:195], s[20:21], 0, v[134:135]
	s_mov_b32 m0, s22
	s_nop 0
	global_load_lds_dwordx4 v[194:195], off
	v_lshl_add_u64 v[194:195], s[20:21], 0, v[138:139]
	s_add_i32 m0, s22, 0x2000
	s_nop 0
	global_load_lds_dwordx4 v[194:195], off
	v_lshl_add_u64 v[194:195], v[232:233], 0, s[94:95]
	s_mov_b32 m0, s41
	s_nop 0
	global_load_lds_dwordx4 v[194:195], off
	v_lshl_add_u64 v[194:195], v[234:235], 0, s[94:95]
	s_mov_b32 m0, s42
	s_nop 0
	global_load_lds_dwordx4 v[194:195], off
	s_waitcnt vmcnt(8)
	s_waitcnt lgkmcnt(0)
	s_barrier
	s_setprio 1
	s_waitcnt lgkmcnt(0)
	v_mfma_f32_16x16x32_bf16 v[64:67], v[146:149], v[178:181], v[64:67]
	v_mfma_f32_16x16x32_bf16 v[60:63], v[154:157], v[178:181], v[60:63]
	v_mfma_f32_16x16x32_bf16 v[48:51], v[146:149], v[186:189], v[48:51]
	v_mfma_f32_16x16x32_bf16 v[44:47], v[154:157], v[186:189], v[44:47]
	v_mfma_f32_16x16x32_bf16 v[32:35], v[146:149], v[204:207], v[32:35]
	v_mfma_f32_16x16x32_bf16 v[28:31], v[154:157], v[204:207], v[28:31]
	v_mfma_f32_16x16x32_bf16 v[16:19], v[146:149], v[212:215], v[16:19]
	v_mfma_f32_16x16x32_bf16 v[12:15], v[154:157], v[212:215], v[12:15]
	v_mfma_f32_16x16x32_bf16 v[64:67], v[150:153], v[182:185], v[64:67]
	v_mfma_f32_16x16x32_bf16 v[60:63], v[158:161], v[182:185], v[60:63]
	v_mfma_f32_16x16x32_bf16 v[48:51], v[150:153], v[190:193], v[48:51]
	v_mfma_f32_16x16x32_bf16 v[44:47], v[158:161], v[190:193], v[44:47]
	v_mfma_f32_16x16x32_bf16 v[32:35], v[150:153], v[208:211], v[32:35]
	v_mfma_f32_16x16x32_bf16 v[28:31], v[158:161], v[208:211], v[28:31]
	v_mfma_f32_16x16x32_bf16 v[16:19], v[150:153], v[226:229], v[16:19]
	v_mfma_f32_16x16x32_bf16 v[12:15], v[158:161], v[226:229], v[12:15]
	s_setprio 0
	s_setprio 1
	v_mfma_f32_16x16x32_bf16 v[56:59], v[162:165], v[178:181], v[56:59]
	v_mfma_f32_16x16x32_bf16 v[52:55], v[170:173], v[178:181], v[52:55]
	v_mfma_f32_16x16x32_bf16 v[40:43], v[162:165], v[186:189], v[40:43]
	v_mfma_f32_16x16x32_bf16 v[36:39], v[170:173], v[186:189], v[36:39]
	v_mfma_f32_16x16x32_bf16 v[24:27], v[162:165], v[204:207], v[24:27]
	v_mfma_f32_16x16x32_bf16 v[20:23], v[170:173], v[204:207], v[20:23]
	v_mfma_f32_16x16x32_bf16 v[8:11], v[162:165], v[212:215], v[8:11]
	v_mfma_f32_16x16x32_bf16 v[4:7], v[170:173], v[212:215], v[4:7]
	v_mfma_f32_16x16x32_bf16 v[56:59], v[166:169], v[182:185], v[56:59]
	v_mfma_f32_16x16x32_bf16 v[52:55], v[174:177], v[182:185], v[52:55]
	v_mfma_f32_16x16x32_bf16 v[40:43], v[166:169], v[190:193], v[40:43]
	v_mfma_f32_16x16x32_bf16 v[36:39], v[174:177], v[190:193], v[36:39]
	v_mfma_f32_16x16x32_bf16 v[24:27], v[166:169], v[208:211], v[24:27]
	v_mfma_f32_16x16x32_bf16 v[20:23], v[174:177], v[208:211], v[20:23]
	v_mfma_f32_16x16x32_bf16 v[8:11], v[166:169], v[226:229], v[8:11]
	v_mfma_f32_16x16x32_bf16 v[4:7], v[174:177], v[226:229], v[4:7]
	s_setprio 0
	s_add_i32 s49, s49, 2
	s_add_u32 s3, s3, 0x100
	s_addc_u32 s46, s46, 0
	s_add_u32 s18, s18, 0x100
	s_addc_u32 s19, s19, 0
	s_cmp_gt_u32 s49, 29
	s_barrier
	s_cbranch_scc0 .LBB0_236
	s_and_b64 vcc, exec, s[10:11]
	s_cbranch_vccz .LBB0_239
	s_barrier

.LBB0_724:
	s_add_u32 s18, s16, 0xfff80080
	s_addc_u32 s19, s17, -1
	s_add_i32 s44, 0, 0x10000
	s_cmp_eq_u32 s43, 28
	s_cselect_b32 s21, s13, s19
	s_cselect_b32 s20, s12, s18
	v_add_u32_e32 v2, s44, v1
	s_cselect_b32 s19, s15, s42
	s_cselect_b32 s18, s14, s7
	s_add_i32 s46, 0, 0x14000
	ds_read_b128 v[146:149], v2
	ds_read_b128 v[150:153], v2 offset:1024
	ds_read_b128 v[154:157], v2 offset:2048
	ds_read_b128 v[158:161], v2 offset:3072
	v_add_u32_e32 v2, s46, v1
	ds_read_b128 v[162:165], v2
	ds_read_b128 v[166:169], v2 offset:1024
	ds_read_b128 v[170:173], v2 offset:2048
	ds_read_b128 v[174:177], v2 offset:3072
	v_lshl_add_u64 v[194:195], s[16:17], 0, v[142:143]
	s_add_i32 m0, s28, 0xc000
	ds_read_b128 v[178:181], v144
	ds_read_b128 v[182:185], v144 offset:1024
	ds_read_b128 v[186:189], v144 offset:2048
	ds_read_b128 v[190:193], v144 offset:3072
	ds_read_b128 v[204:207], v144 offset:4096
	ds_read_b128 v[208:211], v144 offset:5120
	ds_read_b128 v[212:215], v144 offset:6144
	ds_read_b128 v[226:229], v144 offset:7168
	global_load_lds_dwordx4 v[194:195], off
	v_lshl_add_u64 v[194:195], s[16:17], 0, v[140:141]
	s_add_i32 m0, s28, 0xe000
	s_nop 0
	global_load_lds_dwordx4 v[194:195], off
	s_waitcnt vmcnt(8)
	s_waitcnt lgkmcnt(0)
	s_barrier
	s_setprio 1
	s_waitcnt lgkmcnt(0)
	v_mfma_f32_16x16x32_bf16 v[128:131], v[146:149], v[178:181], v[128:131]
	v_mfma_f32_16x16x32_bf16 v[124:127], v[154:157], v[178:181], v[124:127]
	v_mfma_f32_16x16x32_bf16 v[112:115], v[146:149], v[186:189], v[112:115]
	v_mfma_f32_16x16x32_bf16 v[108:111], v[154:157], v[186:189], v[108:111]
	v_mfma_f32_16x16x32_bf16 v[96:99], v[146:149], v[204:207], v[96:99]
	v_mfma_f32_16x16x32_bf16 v[92:95], v[154:157], v[204:207], v[92:95]
	v_mfma_f32_16x16x32_bf16 v[80:83], v[146:149], v[212:215], v[80:83]
	v_mfma_f32_16x16x32_bf16 v[76:79], v[154:157], v[212:215], v[76:79]
	v_mfma_f32_16x16x32_bf16 v[128:131], v[150:153], v[182:185], v[128:131]
	v_mfma_f32_16x16x32_bf16 v[124:127], v[158:161], v[182:185], v[124:127]
	v_mfma_f32_16x16x32_bf16 v[112:115], v[150:153], v[190:193], v[112:115]
	v_mfma_f32_16x16x32_bf16 v[108:111], v[158:161], v[190:193], v[108:111]
	v_mfma_f32_16x16x32_bf16 v[96:99], v[150:153], v[208:211], v[96:99]
	v_mfma_f32_16x16x32_bf16 v[92:95], v[158:161], v[208:211], v[92:95]
	v_mfma_f32_16x16x32_bf16 v[80:83], v[150:153], v[226:229], v[80:83]
	v_mfma_f32_16x16x32_bf16 v[76:79], v[158:161], v[226:229], v[76:79]
	s_setprio 0
	s_setprio 1
	v_mfma_f32_16x16x32_bf16 v[120:123], v[162:165], v[178:181], v[120:123]
	v_mfma_f32_16x16x32_bf16 v[116:119], v[170:173], v[178:181], v[116:119]
	v_mfma_f32_16x16x32_bf16 v[104:107], v[162:165], v[186:189], v[104:107]
	v_mfma_f32_16x16x32_bf16 v[100:103], v[170:173], v[186:189], v[100:103]
	v_mfma_f32_16x16x32_bf16 v[88:91], v[162:165], v[204:207], v[88:91]
	v_mfma_f32_16x16x32_bf16 v[84:87], v[170:173], v[204:207], v[84:87]
	v_mfma_f32_16x16x32_bf16 v[72:75], v[162:165], v[212:215], v[72:75]
	v_mfma_f32_16x16x32_bf16 v[68:71], v[170:173], v[212:215], v[68:71]
	v_mfma_f32_16x16x32_bf16 v[120:123], v[166:169], v[182:185], v[120:123]
	v_mfma_f32_16x16x32_bf16 v[116:119], v[174:177], v[182:185], v[116:119]
	v_mfma_f32_16x16x32_bf16 v[104:107], v[166:169], v[190:193], v[104:107]
	v_mfma_f32_16x16x32_bf16 v[100:103], v[174:177], v[190:193], v[100:103]
	v_mfma_f32_16x16x32_bf16 v[88:91], v[166:169], v[208:211], v[88:91]
	v_mfma_f32_16x16x32_bf16 v[84:87], v[174:177], v[208:211], v[84:87]
	v_mfma_f32_16x16x32_bf16 v[72:75], v[166:169], v[226:229], v[72:75]
	v_mfma_f32_16x16x32_bf16 v[68:71], v[174:177], v[226:229], v[68:71]
	s_setprio 0
	s_barrier
	s_add_i32 s44, s44, s27
	v_lshl_add_u64 v[194:195], s[18:19], 0, v[132:133]
	s_mov_b32 m0, s44
	ds_read_b128 v[178:181], v144 offset:16384
	ds_read_b128 v[182:185], v144 offset:17408
	ds_read_b128 v[186:189], v144 offset:18432
	ds_read_b128 v[190:193], v144 offset:19456
	ds_read_b128 v[204:207], v144 offset:20480
	ds_read_b128 v[208:211], v144 offset:21504
	ds_read_b128 v[212:215], v144 offset:22528
	ds_read_b128 v[226:229], v144 offset:23552
	global_load_lds_dwordx4 v[194:195], off
	s_add_i32 m0, s44, 0x2000
	s_add_u32 s44, s18, 0x80000
	v_lshl_add_u64 v[230:231], s[18:19], 0, v[136:137]
	s_addc_u32 s45, s19, 0
	s_add_i32 s46, s46, s27
	global_load_lds_dwordx4 v[230:231], off
	v_lshl_add_u64 v[232:233], s[44:45], 0, v[132:133]
	s_mov_b32 m0, s46
	v_lshl_add_u64 v[234:235], s[20:21], 0, v[138:139]
	global_load_lds_dwordx4 v[232:233], off
	v_lshl_add_u64 v[232:233], s[44:45], 0, v[136:137]
	s_add_i32 m0, s46, 0x2000
	s_nop 0
	global_load_lds_dwordx4 v[232:233], off
	v_lshl_add_u64 v[232:233], s[20:21], 0, v[134:135]
	s_mov_b32 m0, s28
	s_nop 0
	global_load_lds_dwordx4 v[232:233], off
	s_mov_b32 m0, s29
	s_nop 0
	global_load_lds_dwordx4 v[234:235], off
	s_waitcnt vmcnt(8)
	s_waitcnt lgkmcnt(0)
	s_barrier
	s_setprio 1
	s_waitcnt lgkmcnt(0)
	v_mfma_f32_16x16x32_bf16 v[64:67], v[146:149], v[178:181], v[64:67]
	v_mfma_f32_16x16x32_bf16 v[60:63], v[154:157], v[178:181], v[60:63]
	v_mfma_f32_16x16x32_bf16 v[48:51], v[146:149], v[186:189], v[48:51]
	v_mfma_f32_16x16x32_bf16 v[44:47], v[154:157], v[186:189], v[44:47]
	v_mfma_f32_16x16x32_bf16 v[32:35], v[146:149], v[204:207], v[32:35]
	v_mfma_f32_16x16x32_bf16 v[28:31], v[154:157], v[204:207], v[28:31]
	v_mfma_f32_16x16x32_bf16 v[16:19], v[146:149], v[212:215], v[16:19]
	v_mfma_f32_16x16x32_bf16 v[12:15], v[154:157], v[212:215], v[12:15]
	v_mfma_f32_16x16x32_bf16 v[64:67], v[150:153], v[182:185], v[64:67]
	v_mfma_f32_16x16x32_bf16 v[60:63], v[158:161], v[182:185], v[60:63]
	v_mfma_f32_16x16x32_bf16 v[48:51], v[150:153], v[190:193], v[48:51]
	v_mfma_f32_16x16x32_bf16 v[44:47], v[158:161], v[190:193], v[44:47]
	v_mfma_f32_16x16x32_bf16 v[32:35], v[150:153], v[208:211], v[32:35]
	v_mfma_f32_16x16x32_bf16 v[28:31], v[158:161], v[208:211], v[28:31]
	v_mfma_f32_16x16x32_bf16 v[16:19], v[150:153], v[226:229], v[16:19]
	v_mfma_f32_16x16x32_bf16 v[12:15], v[158:161], v[226:229], v[12:15]
	s_setprio 0
	s_setprio 1
	v_mfma_f32_16x16x32_bf16 v[56:59], v[162:165], v[178:181], v[56:59]
	v_mfma_f32_16x16x32_bf16 v[52:55], v[170:173], v[178:181], v[52:55]
	v_mfma_f32_16x16x32_bf16 v[40:43], v[162:165], v[186:189], v[40:43]
	v_mfma_f32_16x16x32_bf16 v[36:39], v[170:173], v[186:189], v[36:39]
	v_mfma_f32_16x16x32_bf16 v[24:27], v[162:165], v[204:207], v[24:27]
	v_mfma_f32_16x16x32_bf16 v[20:23], v[170:173], v[204:207], v[20:23]
	v_mfma_f32_16x16x32_bf16 v[8:11], v[162:165], v[212:215], v[8:11]
	v_mfma_f32_16x16x32_bf16 v[4:7], v[170:173], v[212:215], v[4:7]
	v_mfma_f32_16x16x32_bf16 v[56:59], v[166:169], v[182:185], v[56:59]
	v_mfma_f32_16x16x32_bf16 v[52:55], v[174:177], v[182:185], v[52:55]
	v_mfma_f32_16x16x32_bf16 v[40:43], v[166:169], v[190:193], v[40:43]
	v_mfma_f32_16x16x32_bf16 v[36:39], v[174:177], v[190:193], v[36:39]
	v_mfma_f32_16x16x32_bf16 v[24:27], v[166:169], v[208:211], v[24:27]
	v_mfma_f32_16x16x32_bf16 v[20:23], v[174:177], v[208:211], v[20:23]
	v_mfma_f32_16x16x32_bf16 v[8:11], v[166:169], v[226:229], v[8:11]
	v_mfma_f32_16x16x32_bf16 v[4:7], v[174:177], v[226:229], v[4:7]
	s_setprio 0
	s_barrier
	s_add_i32 s44, 0, 0x18000
	v_add_u32_e32 v2, s44, v1
	s_add_i32 s45, 0, 0x1c000
	ds_read_b128 v[146:149], v2
	ds_read_b128 v[150:153], v2 offset:1024
	ds_read_b128 v[154:157], v2 offset:2048
	ds_read_b128 v[158:161], v2 offset:3072
	v_add_u32_e32 v2, s45, v1
	ds_read_b128 v[162:165], v2
	ds_read_b128 v[166:169], v2 offset:1024
	ds_read_b128 v[170:173], v2 offset:2048
	ds_read_b128 v[174:177], v2 offset:3072
	s_add_u32 s20, s20, 0x80000
	s_addc_u32 s21, s21, 0
	s_mov_b32 m0, s30
	v_lshl_add_u64 v[236:237], s[20:21], 0, v[134:135]
	ds_read_b128 v[178:181], v144 offset:32768
	ds_read_b128 v[182:185], v144 offset:33792
	ds_read_b128 v[186:189], v144 offset:34816
	ds_read_b128 v[190:193], v144 offset:35840
	ds_read_b128 v[204:207], v144 offset:36864
	ds_read_b128 v[208:211], v144 offset:37888
	ds_read_b128 v[212:215], v144 offset:38912
	ds_read_b128 v[226:229], v144 offset:39936
	global_load_lds_dwordx4 v[236:237], off
	v_lshl_add_u64 v[236:237], s[20:21], 0, v[138:139]
	s_mov_b32 m0, s31
	s_nop 0
	global_load_lds_dwordx4 v[236:237], off
	s_waitcnt vmcnt(8)
	s_waitcnt lgkmcnt(0)
	s_barrier
	s_setprio 1
	s_waitcnt lgkmcnt(0)
	v_mfma_f32_16x16x32_bf16 v[128:131], v[146:149], v[178:181], v[128:131]
	v_mfma_f32_16x16x32_bf16 v[124:127], v[154:157], v[178:181], v[124:127]
	v_mfma_f32_16x16x32_bf16 v[112:115], v[146:149], v[186:189], v[112:115]
	v_mfma_f32_16x16x32_bf16 v[108:111], v[154:157], v[186:189], v[108:111]
	v_mfma_f32_16x16x32_bf16 v[96:99], v[146:149], v[204:207], v[96:99]
	v_mfma_f32_16x16x32_bf16 v[92:95], v[154:157], v[204:207], v[92:95]
	v_mfma_f32_16x16x32_bf16 v[80:83], v[146:149], v[212:215], v[80:83]
	v_mfma_f32_16x16x32_bf16 v[76:79], v[154:157], v[212:215], v[76:79]
	v_mfma_f32_16x16x32_bf16 v[128:131], v[150:153], v[182:185], v[128:131]
	v_mfma_f32_16x16x32_bf16 v[124:127], v[158:161], v[182:185], v[124:127]
	v_mfma_f32_16x16x32_bf16 v[112:115], v[150:153], v[190:193], v[112:115]
	v_mfma_f32_16x16x32_bf16 v[108:111], v[158:161], v[190:193], v[108:111]
	v_mfma_f32_16x16x32_bf16 v[96:99], v[150:153], v[208:211], v[96:99]
	v_mfma_f32_16x16x32_bf16 v[92:95], v[158:161], v[208:211], v[92:95]
	v_mfma_f32_16x16x32_bf16 v[80:83], v[150:153], v[226:229], v[80:83]
	v_mfma_f32_16x16x32_bf16 v[76:79], v[158:161], v[226:229], v[76:79]
	s_setprio 0
	s_setprio 1
	v_mfma_f32_16x16x32_bf16 v[120:123], v[162:165], v[178:181], v[120:123]
	v_mfma_f32_16x16x32_bf16 v[116:119], v[170:173], v[178:181], v[116:119]
	v_mfma_f32_16x16x32_bf16 v[104:107], v[162:165], v[186:189], v[104:107]
	v_mfma_f32_16x16x32_bf16 v[100:103], v[170:173], v[186:189], v[100:103]
	v_mfma_f32_16x16x32_bf16 v[88:91], v[162:165], v[204:207], v[88:91]
	v_mfma_f32_16x16x32_bf16 v[84:87], v[170:173], v[204:207], v[84:87]
	v_mfma_f32_16x16x32_bf16 v[72:75], v[162:165], v[212:215], v[72:75]
	v_mfma_f32_16x16x32_bf16 v[68:71], v[170:173], v[212:215], v[68:71]
	v_mfma_f32_16x16x32_bf16 v[120:123], v[166:169], v[182:185], v[120:123]
	v_mfma_f32_16x16x32_bf16 v[116:119], v[174:177], v[182:185], v[116:119]
	v_mfma_f32_16x16x32_bf16 v[104:107], v[166:169], v[190:193], v[104:107]
	v_mfma_f32_16x16x32_bf16 v[100:103], v[174:177], v[190:193], v[100:103]
	v_mfma_f32_16x16x32_bf16 v[88:91], v[166:169], v[208:211], v[88:91]
	v_mfma_f32_16x16x32_bf16 v[84:87], v[174:177], v[208:211], v[84:87]
	v_mfma_f32_16x16x32_bf16 v[72:75], v[166:169], v[226:229], v[72:75]
	v_mfma_f32_16x16x32_bf16 v[68:71], v[174:177], v[226:229], v[68:71]
	s_setprio 0
	s_barrier
	s_add_i32 s20, s44, s27
	v_lshl_add_u64 v[194:195], v[194:195], 0, s[94:95]
	s_mov_b32 m0, s20
	ds_read_b128 v[178:181], v144 offset:49152
	ds_read_b128 v[182:185], v144 offset:50176
	ds_read_b128 v[186:189], v144 offset:51200
	ds_read_b128 v[190:193], v144 offset:52224
	ds_read_b128 v[204:207], v144 offset:53248
	ds_read_b128 v[208:211], v144 offset:54272
	ds_read_b128 v[212:215], v144 offset:55296
	ds_read_b128 v[226:229], v144 offset:56320
	global_load_lds_dwordx4 v[194:195], off
	s_add_i32 m0, s20, 0x2000
	s_add_u32 s18, s18, 0x80080
	v_lshl_add_u64 v[194:195], v[230:231], 0, s[94:95]
	s_addc_u32 s19, s19, 0
	s_add_i32 s20, s45, s27
	global_load_lds_dwordx4 v[194:195], off
	v_lshl_add_u64 v[194:195], s[18:19], 0, v[132:133]
	s_mov_b32 m0, s20
	s_nop 0
	global_load_lds_dwordx4 v[194:195], off
	v_lshl_add_u64 v[194:195], s[18:19], 0, v[136:137]
	s_add_i32 m0, s20, 0x2000
	s_nop 0
	global_load_lds_dwordx4 v[194:195], off
	v_lshl_add_u64 v[194:195], v[232:233], 0, s[94:95]
	s_mov_b32 m0, s36
	s_nop 0
	global_load_lds_dwordx4 v[194:195], off
	v_lshl_add_u64 v[194:195], v[234:235], 0, s[94:95]
	s_mov_b32 m0, s37
	s_nop 0
	global_load_lds_dwordx4 v[194:195], off
	s_waitcnt vmcnt(8)
	s_waitcnt lgkmcnt(0)
	s_barrier
	s_setprio 1
	s_waitcnt lgkmcnt(0)
	v_mfma_f32_16x16x32_bf16 v[64:67], v[146:149], v[178:181], v[64:67]
	v_mfma_f32_16x16x32_bf16 v[60:63], v[154:157], v[178:181], v[60:63]
	v_mfma_f32_16x16x32_bf16 v[48:51], v[146:149], v[186:189], v[48:51]
	v_mfma_f32_16x16x32_bf16 v[44:47], v[154:157], v[186:189], v[44:47]
	v_mfma_f32_16x16x32_bf16 v[32:35], v[146:149], v[204:207], v[32:35]
	v_mfma_f32_16x16x32_bf16 v[28:31], v[154:157], v[204:207], v[28:31]
	v_mfma_f32_16x16x32_bf16 v[16:19], v[146:149], v[212:215], v[16:19]
	v_mfma_f32_16x16x32_bf16 v[12:15], v[154:157], v[212:215], v[12:15]
	v_mfma_f32_16x16x32_bf16 v[64:67], v[150:153], v[182:185], v[64:67]
	v_mfma_f32_16x16x32_bf16 v[60:63], v[158:161], v[182:185], v[60:63]
	v_mfma_f32_16x16x32_bf16 v[48:51], v[150:153], v[190:193], v[48:51]
	v_mfma_f32_16x16x32_bf16 v[44:47], v[158:161], v[190:193], v[44:47]
	v_mfma_f32_16x16x32_bf16 v[32:35], v[150:153], v[208:211], v[32:35]
	v_mfma_f32_16x16x32_bf16 v[28:31], v[158:161], v[208:211], v[28:31]
	v_mfma_f32_16x16x32_bf16 v[16:19], v[150:153], v[226:229], v[16:19]
	v_mfma_f32_16x16x32_bf16 v[12:15], v[158:161], v[226:229], v[12:15]
	s_setprio 0
	s_setprio 1
	v_mfma_f32_16x16x32_bf16 v[56:59], v[162:165], v[178:181], v[56:59]
	v_mfma_f32_16x16x32_bf16 v[52:55], v[170:173], v[178:181], v[52:55]
	v_mfma_f32_16x16x32_bf16 v[40:43], v[162:165], v[186:189], v[40:43]
	v_mfma_f32_16x16x32_bf16 v[36:39], v[170:173], v[186:189], v[36:39]
	v_mfma_f32_16x16x32_bf16 v[24:27], v[162:165], v[204:207], v[24:27]
	v_mfma_f32_16x16x32_bf16 v[20:23], v[170:173], v[204:207], v[20:23]
	v_mfma_f32_16x16x32_bf16 v[8:11], v[162:165], v[212:215], v[8:11]
	v_mfma_f32_16x16x32_bf16 v[4:7], v[170:173], v[212:215], v[4:7]
	v_mfma_f32_16x16x32_bf16 v[56:59], v[166:169], v[182:185], v[56:59]
	v_mfma_f32_16x16x32_bf16 v[52:55], v[174:177], v[182:185], v[52:55]
	v_mfma_f32_16x16x32_bf16 v[40:43], v[166:169], v[190:193], v[40:43]
	v_mfma_f32_16x16x32_bf16 v[36:39], v[174:177], v[190:193], v[36:39]
	v_mfma_f32_16x16x32_bf16 v[24:27], v[166:169], v[208:211], v[24:27]
	v_mfma_f32_16x16x32_bf16 v[20:23], v[174:177], v[208:211], v[20:23]
	v_mfma_f32_16x16x32_bf16 v[8:11], v[166:169], v[226:229], v[8:11]
	v_mfma_f32_16x16x32_bf16 v[4:7], v[174:177], v[226:229], v[4:7]
	s_setprio 0
	s_add_i32 s43, s43, 2
	s_add_u32 s7, s7, 0x100
	s_addc_u32 s42, s42, 0
	s_add_u32 s16, s16, 0x100
	s_addc_u32 s17, s17, 0
	s_cmp_gt_u32 s43, 29
	s_barrier
	s_cbranch_scc0 .LBB0_724
	s_and_b64 vcc, exec, s[10:11]
	s_cbranch_vccz .LBB0_727
	s_barrier

.LBB0_909:
	s_add_u32 s22, s4, 0xfff80080
	s_addc_u32 s23, s5, -1
	s_add_i32 s55, 0, 0x10000
	s_cmp_eq_u32 s54, 28
	s_cselect_b32 s25, s19, s23
	s_cselect_b32 s24, s18, s22
	v_add_u32_e32 v2, s55, v1
	s_cselect_b32 s23, s21, s53
	s_cselect_b32 s22, s20, s52
	s_add_i32 s58, 0, 0x14000
	ds_read_b128 v[132:135], v2
	ds_read_b128 v[136:139], v2 offset:1024
	ds_read_b128 v[152:155], v2 offset:2048
	ds_read_b128 v[156:159], v2 offset:3072
	v_add_u32_e32 v2, s58, v1
	ds_read_b128 v[164:167], v2
	ds_read_b128 v[168:171], v2 offset:1024
	ds_read_b128 v[172:175], v2 offset:2048
	ds_read_b128 v[176:179], v2 offset:3072
	v_lshl_add_u64 v[160:161], s[4:5], 0, v[150:151]
	s_add_i32 m0, s35, 0xc000
	ds_read_b128 v[180:183], v162
	ds_read_b128 v[184:187], v162 offset:1024
	ds_read_b128 v[188:191], v162 offset:2048
	ds_read_b128 v[192:195], v162 offset:3072
	ds_read_b128 v[204:207], v162 offset:4096
	ds_read_b128 v[208:211], v162 offset:5120
	ds_read_b128 v[212:215], v162 offset:6144
	ds_read_b128 v[226:229], v162 offset:7168
	global_load_lds_dwordx4 v[160:161], off
	v_lshl_add_u64 v[160:161], s[4:5], 0, v[148:149]
	s_add_i32 m0, s35, 0xe000
	s_nop 0
	global_load_lds_dwordx4 v[160:161], off
	s_waitcnt vmcnt(8)
	s_waitcnt lgkmcnt(0)
	s_barrier
	s_setprio 1
	s_waitcnt lgkmcnt(0)
	v_mfma_f32_16x16x32_bf16 v[128:131], v[132:135], v[180:183], v[128:131]
	v_mfma_f32_16x16x32_bf16 v[124:127], v[152:155], v[180:183], v[124:127]
	v_mfma_f32_16x16x32_bf16 v[112:115], v[132:135], v[188:191], v[112:115]
	v_mfma_f32_16x16x32_bf16 v[108:111], v[152:155], v[188:191], v[108:111]
	v_mfma_f32_16x16x32_bf16 v[96:99], v[132:135], v[204:207], v[96:99]
	v_mfma_f32_16x16x32_bf16 v[92:95], v[152:155], v[204:207], v[92:95]
	v_mfma_f32_16x16x32_bf16 v[80:83], v[132:135], v[212:215], v[80:83]
	v_mfma_f32_16x16x32_bf16 v[76:79], v[152:155], v[212:215], v[76:79]
	v_mfma_f32_16x16x32_bf16 v[128:131], v[136:139], v[184:187], v[128:131]
	v_mfma_f32_16x16x32_bf16 v[124:127], v[156:159], v[184:187], v[124:127]
	v_mfma_f32_16x16x32_bf16 v[112:115], v[136:139], v[192:195], v[112:115]
	v_mfma_f32_16x16x32_bf16 v[108:111], v[156:159], v[192:195], v[108:111]
	v_mfma_f32_16x16x32_bf16 v[96:99], v[136:139], v[208:211], v[96:99]
	v_mfma_f32_16x16x32_bf16 v[92:95], v[156:159], v[208:211], v[92:95]
	v_mfma_f32_16x16x32_bf16 v[80:83], v[136:139], v[226:229], v[80:83]
	v_mfma_f32_16x16x32_bf16 v[76:79], v[156:159], v[226:229], v[76:79]
	s_setprio 0
	s_setprio 1
	v_mfma_f32_16x16x32_bf16 v[120:123], v[164:167], v[180:183], v[120:123]
	v_mfma_f32_16x16x32_bf16 v[116:119], v[172:175], v[180:183], v[116:119]
	v_mfma_f32_16x16x32_bf16 v[104:107], v[164:167], v[188:191], v[104:107]
	v_mfma_f32_16x16x32_bf16 v[100:103], v[172:175], v[188:191], v[100:103]
	v_mfma_f32_16x16x32_bf16 v[88:91], v[164:167], v[204:207], v[88:91]
	v_mfma_f32_16x16x32_bf16 v[84:87], v[172:175], v[204:207], v[84:87]
	v_mfma_f32_16x16x32_bf16 v[72:75], v[164:167], v[212:215], v[72:75]
	v_mfma_f32_16x16x32_bf16 v[68:71], v[172:175], v[212:215], v[68:71]
	v_mfma_f32_16x16x32_bf16 v[120:123], v[168:171], v[184:187], v[120:123]
	v_mfma_f32_16x16x32_bf16 v[116:119], v[176:179], v[184:187], v[116:119]
	v_mfma_f32_16x16x32_bf16 v[104:107], v[168:171], v[192:195], v[104:107]
	v_mfma_f32_16x16x32_bf16 v[100:103], v[176:179], v[192:195], v[100:103]
	v_mfma_f32_16x16x32_bf16 v[88:91], v[168:171], v[208:211], v[88:91]
	v_mfma_f32_16x16x32_bf16 v[84:87], v[176:179], v[208:211], v[84:87]
	v_mfma_f32_16x16x32_bf16 v[72:75], v[168:171], v[226:229], v[72:75]
	v_mfma_f32_16x16x32_bf16 v[68:71], v[176:179], v[226:229], v[68:71]
	s_setprio 0
	s_barrier
	s_add_i32 s55, s55, s34
	v_lshl_add_u64 v[160:161], s[22:23], 0, v[140:141]
	s_mov_b32 m0, s55
	ds_read_b128 v[180:183], v162 offset:16384
	ds_read_b128 v[184:187], v162 offset:17408
	ds_read_b128 v[188:191], v162 offset:18432
	ds_read_b128 v[192:195], v162 offset:19456
	ds_read_b128 v[204:207], v162 offset:20480
	ds_read_b128 v[208:211], v162 offset:21504
	ds_read_b128 v[212:215], v162 offset:22528
	ds_read_b128 v[226:229], v162 offset:23552
	global_load_lds_dwordx4 v[160:161], off
	s_add_i32 m0, s55, 0x2000
	s_add_u32 s56, s22, 0x80000
	v_lshl_add_u64 v[230:231], s[22:23], 0, v[144:145]
	s_addc_u32 s57, s23, 0
	s_add_i32 s55, s58, s34
	global_load_lds_dwordx4 v[230:231], off
	v_lshl_add_u64 v[232:233], s[56:57], 0, v[140:141]
	s_mov_b32 m0, s55
	v_lshl_add_u64 v[234:235], s[24:25], 0, v[146:147]
	global_load_lds_dwordx4 v[232:233], off
	v_lshl_add_u64 v[232:233], s[56:57], 0, v[144:145]
	s_add_i32 m0, s55, 0x2000
	s_nop 0
	global_load_lds_dwordx4 v[232:233], off
	v_lshl_add_u64 v[232:233], s[24:25], 0, v[142:143]
	s_mov_b32 m0, s35
	s_nop 0
	global_load_lds_dwordx4 v[232:233], off
	s_mov_b32 m0, s36
	s_nop 0
	global_load_lds_dwordx4 v[234:235], off
	s_waitcnt vmcnt(8)
	s_waitcnt lgkmcnt(0)
	s_barrier
	s_setprio 1
	s_waitcnt lgkmcnt(0)
	v_mfma_f32_16x16x32_bf16 v[64:67], v[132:135], v[180:183], v[64:67]
	v_mfma_f32_16x16x32_bf16 v[60:63], v[152:155], v[180:183], v[60:63]
	v_mfma_f32_16x16x32_bf16 v[48:51], v[132:135], v[188:191], v[48:51]
	v_mfma_f32_16x16x32_bf16 v[44:47], v[152:155], v[188:191], v[44:47]
	v_mfma_f32_16x16x32_bf16 v[32:35], v[132:135], v[204:207], v[32:35]
	v_mfma_f32_16x16x32_bf16 v[28:31], v[152:155], v[204:207], v[28:31]
	v_mfma_f32_16x16x32_bf16 v[16:19], v[132:135], v[212:215], v[16:19]
	v_mfma_f32_16x16x32_bf16 v[12:15], v[152:155], v[212:215], v[12:15]
	v_mfma_f32_16x16x32_bf16 v[64:67], v[136:139], v[184:187], v[64:67]
	v_mfma_f32_16x16x32_bf16 v[60:63], v[156:159], v[184:187], v[60:63]
	v_mfma_f32_16x16x32_bf16 v[48:51], v[136:139], v[192:195], v[48:51]
	v_mfma_f32_16x16x32_bf16 v[44:47], v[156:159], v[192:195], v[44:47]
	v_mfma_f32_16x16x32_bf16 v[32:35], v[136:139], v[208:211], v[32:35]
	v_mfma_f32_16x16x32_bf16 v[28:31], v[156:159], v[208:211], v[28:31]
	v_mfma_f32_16x16x32_bf16 v[16:19], v[136:139], v[226:229], v[16:19]
	v_mfma_f32_16x16x32_bf16 v[12:15], v[156:159], v[226:229], v[12:15]
	s_setprio 0
	s_setprio 1
	v_mfma_f32_16x16x32_bf16 v[56:59], v[164:167], v[180:183], v[56:59]
	v_mfma_f32_16x16x32_bf16 v[52:55], v[172:175], v[180:183], v[52:55]
	v_mfma_f32_16x16x32_bf16 v[40:43], v[164:167], v[188:191], v[40:43]
	v_mfma_f32_16x16x32_bf16 v[36:39], v[172:175], v[188:191], v[36:39]
	v_mfma_f32_16x16x32_bf16 v[24:27], v[164:167], v[204:207], v[24:27]
	v_mfma_f32_16x16x32_bf16 v[20:23], v[172:175], v[204:207], v[20:23]
	v_mfma_f32_16x16x32_bf16 v[8:11], v[164:167], v[212:215], v[8:11]
	v_mfma_f32_16x16x32_bf16 v[4:7], v[172:175], v[212:215], v[4:7]
	v_mfma_f32_16x16x32_bf16 v[56:59], v[168:171], v[184:187], v[56:59]
	v_mfma_f32_16x16x32_bf16 v[52:55], v[176:179], v[184:187], v[52:55]
	v_mfma_f32_16x16x32_bf16 v[40:43], v[168:171], v[192:195], v[40:43]
	v_mfma_f32_16x16x32_bf16 v[36:39], v[176:179], v[192:195], v[36:39]
	v_mfma_f32_16x16x32_bf16 v[24:27], v[168:171], v[208:211], v[24:27]
	v_mfma_f32_16x16x32_bf16 v[20:23], v[176:179], v[208:211], v[20:23]
	v_mfma_f32_16x16x32_bf16 v[8:11], v[168:171], v[226:229], v[8:11]
	v_mfma_f32_16x16x32_bf16 v[4:7], v[176:179], v[226:229], v[4:7]
	s_setprio 0
	s_barrier
	s_add_i32 s55, 0, 0x18000
	v_add_u32_e32 v2, s55, v1
	s_add_i32 s56, 0, 0x1c000
	ds_read_b128 v[132:135], v2
	ds_read_b128 v[136:139], v2 offset:1024
	ds_read_b128 v[152:155], v2 offset:2048
	ds_read_b128 v[156:159], v2 offset:3072
	v_add_u32_e32 v2, s56, v1
	ds_read_b128 v[164:167], v2
	ds_read_b128 v[168:171], v2 offset:1024
	ds_read_b128 v[172:175], v2 offset:2048
	ds_read_b128 v[176:179], v2 offset:3072
	s_add_u32 s24, s24, 0x80000
	s_addc_u32 s25, s25, 0
	s_mov_b32 m0, s37
	v_lshl_add_u64 v[236:237], s[24:25], 0, v[142:143]
	ds_read_b128 v[180:183], v162 offset:32768
	ds_read_b128 v[184:187], v162 offset:33792
	ds_read_b128 v[188:191], v162 offset:34816
	ds_read_b128 v[192:195], v162 offset:35840
	ds_read_b128 v[204:207], v162 offset:36864
	ds_read_b128 v[208:211], v162 offset:37888
	ds_read_b128 v[212:215], v162 offset:38912
	ds_read_b128 v[226:229], v162 offset:39936
	global_load_lds_dwordx4 v[236:237], off
	v_lshl_add_u64 v[236:237], s[24:25], 0, v[146:147]
	s_mov_b32 m0, s38
	s_nop 0
	global_load_lds_dwordx4 v[236:237], off
	s_waitcnt vmcnt(8)
	s_waitcnt lgkmcnt(0)
	s_barrier
	s_setprio 1
	s_waitcnt lgkmcnt(0)
	v_mfma_f32_16x16x32_bf16 v[128:131], v[132:135], v[180:183], v[128:131]
	v_mfma_f32_16x16x32_bf16 v[124:127], v[152:155], v[180:183], v[124:127]
	v_mfma_f32_16x16x32_bf16 v[112:115], v[132:135], v[188:191], v[112:115]
	v_mfma_f32_16x16x32_bf16 v[108:111], v[152:155], v[188:191], v[108:111]
	v_mfma_f32_16x16x32_bf16 v[96:99], v[132:135], v[204:207], v[96:99]
	v_mfma_f32_16x16x32_bf16 v[92:95], v[152:155], v[204:207], v[92:95]
	v_mfma_f32_16x16x32_bf16 v[80:83], v[132:135], v[212:215], v[80:83]
	v_mfma_f32_16x16x32_bf16 v[76:79], v[152:155], v[212:215], v[76:79]
	v_mfma_f32_16x16x32_bf16 v[128:131], v[136:139], v[184:187], v[128:131]
	v_mfma_f32_16x16x32_bf16 v[124:127], v[156:159], v[184:187], v[124:127]
	v_mfma_f32_16x16x32_bf16 v[112:115], v[136:139], v[192:195], v[112:115]
	v_mfma_f32_16x16x32_bf16 v[108:111], v[156:159], v[192:195], v[108:111]
	v_mfma_f32_16x16x32_bf16 v[96:99], v[136:139], v[208:211], v[96:99]
	v_mfma_f32_16x16x32_bf16 v[92:95], v[156:159], v[208:211], v[92:95]
	v_mfma_f32_16x16x32_bf16 v[80:83], v[136:139], v[226:229], v[80:83]
	v_mfma_f32_16x16x32_bf16 v[76:79], v[156:159], v[226:229], v[76:79]
	s_setprio 0
	s_setprio 1
	v_mfma_f32_16x16x32_bf16 v[120:123], v[164:167], v[180:183], v[120:123]
	v_mfma_f32_16x16x32_bf16 v[116:119], v[172:175], v[180:183], v[116:119]
	v_mfma_f32_16x16x32_bf16 v[104:107], v[164:167], v[188:191], v[104:107]
	v_mfma_f32_16x16x32_bf16 v[100:103], v[172:175], v[188:191], v[100:103]
	v_mfma_f32_16x16x32_bf16 v[88:91], v[164:167], v[204:207], v[88:91]
	v_mfma_f32_16x16x32_bf16 v[84:87], v[172:175], v[204:207], v[84:87]
	v_mfma_f32_16x16x32_bf16 v[72:75], v[164:167], v[212:215], v[72:75]
	v_mfma_f32_16x16x32_bf16 v[68:71], v[172:175], v[212:215], v[68:71]
	v_mfma_f32_16x16x32_bf16 v[120:123], v[168:171], v[184:187], v[120:123]
	v_mfma_f32_16x16x32_bf16 v[116:119], v[176:179], v[184:187], v[116:119]
	v_mfma_f32_16x16x32_bf16 v[104:107], v[168:171], v[192:195], v[104:107]
	v_mfma_f32_16x16x32_bf16 v[100:103], v[176:179], v[192:195], v[100:103]
	v_mfma_f32_16x16x32_bf16 v[88:91], v[168:171], v[208:211], v[88:91]
	v_mfma_f32_16x16x32_bf16 v[84:87], v[176:179], v[208:211], v[84:87]
	v_mfma_f32_16x16x32_bf16 v[72:75], v[168:171], v[226:229], v[72:75]
	v_mfma_f32_16x16x32_bf16 v[68:71], v[176:179], v[226:229], v[68:71]
	s_setprio 0
	s_barrier
	s_add_i32 s24, s55, s34
	v_lshl_add_u64 v[160:161], v[160:161], 0, s[94:95]
	s_mov_b32 m0, s24
	ds_read_b128 v[180:183], v162 offset:49152
	ds_read_b128 v[184:187], v162 offset:50176
	ds_read_b128 v[188:191], v162 offset:51200
	ds_read_b128 v[192:195], v162 offset:52224
	ds_read_b128 v[204:207], v162 offset:53248
	ds_read_b128 v[208:211], v162 offset:54272
	ds_read_b128 v[212:215], v162 offset:55296
	ds_read_b128 v[226:229], v162 offset:56320
	global_load_lds_dwordx4 v[160:161], off
	s_add_i32 m0, s24, 0x2000
	s_add_u32 s22, s22, 0x80080
	v_lshl_add_u64 v[160:161], v[230:231], 0, s[94:95]
	s_addc_u32 s23, s23, 0
	s_add_i32 s24, s56, s34
	global_load_lds_dwordx4 v[160:161], off
	v_lshl_add_u64 v[160:161], s[22:23], 0, v[140:141]
	s_mov_b32 m0, s24
	s_nop 0
	global_load_lds_dwordx4 v[160:161], off
	v_lshl_add_u64 v[160:161], s[22:23], 0, v[144:145]
	s_add_i32 m0, s24, 0x2000
	s_nop 0
	global_load_lds_dwordx4 v[160:161], off
	v_lshl_add_u64 v[160:161], v[232:233], 0, s[94:95]
	s_mov_b32 m0, s42
	s_nop 0
	global_load_lds_dwordx4 v[160:161], off
	v_lshl_add_u64 v[160:161], v[234:235], 0, s[94:95]
	s_mov_b32 m0, s43
	s_nop 0
	global_load_lds_dwordx4 v[160:161], off
	s_waitcnt vmcnt(8)
	s_waitcnt lgkmcnt(0)
	s_barrier
	s_setprio 1
	s_waitcnt lgkmcnt(0)
	v_mfma_f32_16x16x32_bf16 v[64:67], v[132:135], v[180:183], v[64:67]
	v_mfma_f32_16x16x32_bf16 v[60:63], v[152:155], v[180:183], v[60:63]
	v_mfma_f32_16x16x32_bf16 v[48:51], v[132:135], v[188:191], v[48:51]
	v_mfma_f32_16x16x32_bf16 v[44:47], v[152:155], v[188:191], v[44:47]
	v_mfma_f32_16x16x32_bf16 v[32:35], v[132:135], v[204:207], v[32:35]
	v_mfma_f32_16x16x32_bf16 v[28:31], v[152:155], v[204:207], v[28:31]
	v_mfma_f32_16x16x32_bf16 v[16:19], v[132:135], v[212:215], v[16:19]
	v_mfma_f32_16x16x32_bf16 v[12:15], v[152:155], v[212:215], v[12:15]
	v_mfma_f32_16x16x32_bf16 v[64:67], v[136:139], v[184:187], v[64:67]
	v_mfma_f32_16x16x32_bf16 v[60:63], v[156:159], v[184:187], v[60:63]
	v_mfma_f32_16x16x32_bf16 v[48:51], v[136:139], v[192:195], v[48:51]
	v_mfma_f32_16x16x32_bf16 v[44:47], v[156:159], v[192:195], v[44:47]
	v_mfma_f32_16x16x32_bf16 v[32:35], v[136:139], v[208:211], v[32:35]
	v_mfma_f32_16x16x32_bf16 v[28:31], v[156:159], v[208:211], v[28:31]
	v_mfma_f32_16x16x32_bf16 v[16:19], v[136:139], v[226:229], v[16:19]
	v_mfma_f32_16x16x32_bf16 v[12:15], v[156:159], v[226:229], v[12:15]
	s_setprio 0
	s_setprio 1
	v_mfma_f32_16x16x32_bf16 v[56:59], v[164:167], v[180:183], v[56:59]
	v_mfma_f32_16x16x32_bf16 v[52:55], v[172:175], v[180:183], v[52:55]
	v_mfma_f32_16x16x32_bf16 v[40:43], v[164:167], v[188:191], v[40:43]
	v_mfma_f32_16x16x32_bf16 v[36:39], v[172:175], v[188:191], v[36:39]
	v_mfma_f32_16x16x32_bf16 v[24:27], v[164:167], v[204:207], v[24:27]
	v_mfma_f32_16x16x32_bf16 v[20:23], v[172:175], v[204:207], v[20:23]
	v_mfma_f32_16x16x32_bf16 v[8:11], v[164:167], v[212:215], v[8:11]
	v_mfma_f32_16x16x32_bf16 v[4:7], v[172:175], v[212:215], v[4:7]
	v_mfma_f32_16x16x32_bf16 v[56:59], v[168:171], v[184:187], v[56:59]
	v_mfma_f32_16x16x32_bf16 v[52:55], v[176:179], v[184:187], v[52:55]
	v_mfma_f32_16x16x32_bf16 v[40:43], v[168:171], v[192:195], v[40:43]
	v_mfma_f32_16x16x32_bf16 v[36:39], v[176:179], v[192:195], v[36:39]
	v_mfma_f32_16x16x32_bf16 v[24:27], v[168:171], v[208:211], v[24:27]
	v_mfma_f32_16x16x32_bf16 v[20:23], v[176:179], v[208:211], v[20:23]
	v_mfma_f32_16x16x32_bf16 v[8:11], v[168:171], v[226:229], v[8:11]
	v_mfma_f32_16x16x32_bf16 v[4:7], v[176:179], v[226:229], v[4:7]
	s_setprio 0
	s_add_i32 s54, s54, 2
	s_add_u32 s52, s52, 0x100
	s_addc_u32 s53, s53, 0
	s_add_u32 s4, s4, 0x100
	s_addc_u32 s5, s5, 0
	s_cmp_gt_u32 s54, 29
	s_barrier
	s_cbranch_scc0 .LBB0_909
	s_and_b64 vcc, exec, s[14:15]
	s_cbranch_vccz .LBB0_912
	s_barrier

.LBB0_2674:
	s_add_u32 s40, s26, s34
	s_addc_u32 s41, s27, s35
	s_add_u32 s38, s40, 0x100
	s_addc_u32 s39, s41, 0
	v_cndmask_b32_e64 v2, 0, 1, s[36:37]
	s_and_b64 s[36:37], s[30:31], exec
	s_cselect_b32 s37, s19, s39
	s_cselect_b32 s36, s25, s38
	s_add_u32 s34, s28, s34
	s_addc_u32 s35, s29, s35
	s_add_u32 s34, s34, 0x100
	s_addc_u32 s35, s35, 0
	s_add_i32 s73, 0, 0x10000
	s_and_b64 s[30:31], s[30:31], exec
	s_cselect_b32 s39, s46, s35
	s_cselect_b32 s38, s64, s34
	s_add_i32 s31, 0, 0x14000
	s_add_u32 s42, s40, 0x10080
	s_addc_u32 s43, s41, 0
	s_add_i32 s72, s73, s53
	s_add_i32 m0, s54, 0xc000
	s_add_i32 s76, s54, 0xe000
	s_add_i32 s69, s72, 0x2000
	v_add_u32_e32 v144, s73, v1
	s_add_u32 s40, s38, 0x10000
	ds_read_b128 v[132:135], v144
	ds_read_b128 v[148:151], v144 offset:1024
	ds_read_b128 v[152:155], v144 offset:2048
	ds_read_b128 v[156:159], v144 offset:3072
	v_add_u32_e32 v144, s31, v1
	s_addc_u32 s41, s39, 0
	s_add_i32 s71, s31, s53
	ds_read_b128 v[160:163], v144
	ds_read_b128 v[164:167], v144 offset:1024
	ds_read_b128 v[168:171], v144 offset:2048
	ds_read_b128 v[172:175], v144 offset:3072
	s_add_i32 s70, s71, 0x2000
	s_add_i32 s68, 0, 0x18000
	s_add_i32 s67, 0, 0x1c000
	s_add_u32 s34, s36, 0x10000
	s_addc_u32 s35, s37, 0
	s_add_i32 s66, s68, s53
	s_add_i32 s65, s66, 0x2000
	s_add_u32 s30, s38, 0x10080
	s_addc_u32 s31, s39, 0
	s_add_i32 s75, s67, s53
	s_add_i32 s73, s75, 0x2000
	v_cmp_ne_u32_e32 vcc, 1, v2
	v_lshl_add_u64 v[144:145], s[42:43], 0, v[138:139]
	ds_read_b128 v[176:179], v146
	ds_read_b128 v[180:183], v146 offset:1024
	ds_read_b128 v[184:187], v146 offset:2048
	ds_read_b128 v[188:191], v146 offset:3072
	ds_read_b128 v[192:195], v146 offset:4096
	ds_read_b128 v[204:207], v146 offset:5120
	ds_read_b128 v[208:211], v146 offset:6144
	ds_read_b128 v[212:215], v146 offset:7168
	global_load_lds_dwordx4 v[144:145], off
	v_lshl_add_u64 v[144:145], s[42:43], 0, v[142:143]
	s_mov_b32 m0, s76
	s_nop 0
	global_load_lds_dwordx4 v[144:145], off
	s_waitcnt vmcnt(8)
	s_waitcnt lgkmcnt(0)
	s_barrier
	s_setprio 1
	s_waitcnt lgkmcnt(0)
	v_mfma_f32_16x16x32_bf16 v[128:131], v[132:135], v[176:179], v[128:131]
	v_mfma_f32_16x16x32_bf16 v[124:127], v[152:155], v[176:179], v[124:127]
	v_mfma_f32_16x16x32_bf16 v[116:119], v[132:135], v[184:187], v[116:119]
	v_mfma_f32_16x16x32_bf16 v[108:111], v[152:155], v[184:187], v[108:111]
	v_mfma_f32_16x16x32_bf16 v[100:103], v[132:135], v[192:195], v[100:103]
	v_mfma_f32_16x16x32_bf16 v[92:95], v[152:155], v[192:195], v[92:95]
	v_mfma_f32_16x16x32_bf16 v[84:87], v[132:135], v[208:211], v[84:87]
	v_mfma_f32_16x16x32_bf16 v[76:79], v[152:155], v[208:211], v[76:79]
	v_mfma_f32_16x16x32_bf16 v[128:131], v[148:151], v[180:183], v[128:131]
	v_mfma_f32_16x16x32_bf16 v[124:127], v[156:159], v[180:183], v[124:127]
	v_mfma_f32_16x16x32_bf16 v[116:119], v[148:151], v[188:191], v[116:119]
	v_mfma_f32_16x16x32_bf16 v[108:111], v[156:159], v[188:191], v[108:111]
	v_mfma_f32_16x16x32_bf16 v[100:103], v[148:151], v[204:207], v[100:103]
	v_mfma_f32_16x16x32_bf16 v[92:95], v[156:159], v[204:207], v[92:95]
	v_mfma_f32_16x16x32_bf16 v[84:87], v[148:151], v[212:215], v[84:87]
	v_mfma_f32_16x16x32_bf16 v[76:79], v[156:159], v[212:215], v[76:79]
	s_setprio 0
	s_setprio 1
	v_mfma_f32_16x16x32_bf16 v[120:123], v[160:163], v[176:179], v[120:123]
	v_mfma_f32_16x16x32_bf16 v[112:115], v[168:171], v[176:179], v[112:115]
	v_mfma_f32_16x16x32_bf16 v[104:107], v[160:163], v[184:187], v[104:107]
	v_mfma_f32_16x16x32_bf16 v[96:99], v[168:171], v[184:187], v[96:99]
	v_mfma_f32_16x16x32_bf16 v[88:91], v[160:163], v[192:195], v[88:91]
	v_mfma_f32_16x16x32_bf16 v[80:83], v[168:171], v[192:195], v[80:83]
	v_mfma_f32_16x16x32_bf16 v[72:75], v[160:163], v[208:211], v[72:75]
	v_mfma_f32_16x16x32_bf16 v[68:71], v[168:171], v[208:211], v[68:71]
	v_mfma_f32_16x16x32_bf16 v[120:123], v[164:167], v[180:183], v[120:123]
	v_mfma_f32_16x16x32_bf16 v[112:115], v[172:175], v[180:183], v[112:115]
	v_mfma_f32_16x16x32_bf16 v[104:107], v[164:167], v[188:191], v[104:107]
	v_mfma_f32_16x16x32_bf16 v[96:99], v[172:175], v[188:191], v[96:99]
	v_mfma_f32_16x16x32_bf16 v[88:91], v[164:167], v[204:207], v[88:91]
	v_mfma_f32_16x16x32_bf16 v[80:83], v[172:175], v[204:207], v[80:83]
	v_mfma_f32_16x16x32_bf16 v[72:75], v[164:167], v[212:215], v[72:75]
	v_mfma_f32_16x16x32_bf16 v[68:71], v[172:175], v[212:215], v[68:71]
	s_setprio 0
	s_barrier
	s_mov_b32 m0, s72
	v_lshl_add_u64 v[144:145], s[38:39], 0, v[136:137]
	ds_read_b128 v[176:179], v146 offset:16384
	ds_read_b128 v[180:183], v146 offset:17408
	ds_read_b128 v[184:187], v146 offset:18432
	ds_read_b128 v[188:191], v146 offset:19456
	ds_read_b128 v[192:195], v146 offset:20480
	ds_read_b128 v[204:207], v146 offset:21504
	ds_read_b128 v[208:211], v146 offset:22528
	ds_read_b128 v[212:215], v146 offset:23552
	global_load_lds_dwordx4 v[144:145], off
	v_lshl_add_u64 v[226:227], s[38:39], 0, v[140:141]
	s_mov_b32 m0, s69
	v_lshl_add_u64 v[228:229], s[40:41], 0, v[136:137]
	global_load_lds_dwordx4 v[226:227], off
	s_mov_b32 m0, s71
	v_lshl_add_u64 v[230:231], s[36:37], 0, v[142:143]
	global_load_lds_dwordx4 v[228:229], off
	v_lshl_add_u64 v[228:229], s[40:41], 0, v[140:141]
	s_mov_b32 m0, s70
	s_nop 0
	global_load_lds_dwordx4 v[228:229], off
	v_lshl_add_u64 v[228:229], s[36:37], 0, v[138:139]
	s_mov_b32 m0, s54
	s_nop 0
	global_load_lds_dwordx4 v[228:229], off
	s_mov_b32 m0, s55
	s_nop 0
	global_load_lds_dwordx4 v[230:231], off
	s_waitcnt vmcnt(8)
	s_waitcnt lgkmcnt(0)
	s_barrier
	s_setprio 1
	s_waitcnt lgkmcnt(0)
	v_mfma_f32_16x16x32_bf16 v[64:67], v[132:135], v[176:179], v[64:67]
	v_mfma_f32_16x16x32_bf16 v[60:63], v[152:155], v[176:179], v[60:63]
	v_mfma_f32_16x16x32_bf16 v[52:55], v[132:135], v[184:187], v[52:55]
	v_mfma_f32_16x16x32_bf16 v[44:47], v[152:155], v[184:187], v[44:47]
	v_mfma_f32_16x16x32_bf16 v[36:39], v[132:135], v[192:195], v[36:39]
	v_mfma_f32_16x16x32_bf16 v[28:31], v[152:155], v[192:195], v[28:31]
	v_mfma_f32_16x16x32_bf16 v[20:23], v[132:135], v[208:211], v[20:23]
	v_mfma_f32_16x16x32_bf16 v[12:15], v[152:155], v[208:211], v[12:15]
	v_mfma_f32_16x16x32_bf16 v[64:67], v[148:151], v[180:183], v[64:67]
	v_mfma_f32_16x16x32_bf16 v[60:63], v[156:159], v[180:183], v[60:63]
	v_mfma_f32_16x16x32_bf16 v[52:55], v[148:151], v[188:191], v[52:55]
	v_mfma_f32_16x16x32_bf16 v[44:47], v[156:159], v[188:191], v[44:47]
	v_mfma_f32_16x16x32_bf16 v[36:39], v[148:151], v[204:207], v[36:39]
	v_mfma_f32_16x16x32_bf16 v[28:31], v[156:159], v[204:207], v[28:31]
	v_mfma_f32_16x16x32_bf16 v[20:23], v[148:151], v[212:215], v[20:23]
	v_mfma_f32_16x16x32_bf16 v[12:15], v[156:159], v[212:215], v[12:15]
	s_setprio 0
	s_setprio 1
	v_mfma_f32_16x16x32_bf16 v[56:59], v[160:163], v[176:179], v[56:59]
	v_mfma_f32_16x16x32_bf16 v[48:51], v[168:171], v[176:179], v[48:51]
	v_mfma_f32_16x16x32_bf16 v[40:43], v[160:163], v[184:187], v[40:43]
	v_mfma_f32_16x16x32_bf16 v[32:35], v[168:171], v[184:187], v[32:35]
	v_mfma_f32_16x16x32_bf16 v[24:27], v[160:163], v[192:195], v[24:27]
	v_mfma_f32_16x16x32_bf16 v[16:19], v[168:171], v[192:195], v[16:19]
	v_mfma_f32_16x16x32_bf16 v[8:11], v[160:163], v[208:211], v[8:11]
	v_mfma_f32_16x16x32_bf16 v[4:7], v[168:171], v[208:211], v[4:7]
	v_mfma_f32_16x16x32_bf16 v[56:59], v[164:167], v[180:183], v[56:59]
	v_mfma_f32_16x16x32_bf16 v[48:51], v[172:175], v[180:183], v[48:51]
	v_mfma_f32_16x16x32_bf16 v[40:43], v[164:167], v[188:191], v[40:43]
	v_mfma_f32_16x16x32_bf16 v[32:35], v[172:175], v[188:191], v[32:35]
	v_mfma_f32_16x16x32_bf16 v[24:27], v[164:167], v[204:207], v[24:27]
	v_mfma_f32_16x16x32_bf16 v[16:19], v[172:175], v[204:207], v[16:19]
	v_mfma_f32_16x16x32_bf16 v[8:11], v[164:167], v[212:215], v[8:11]
	v_mfma_f32_16x16x32_bf16 v[4:7], v[172:175], v[212:215], v[4:7]
	s_setprio 0
	s_barrier
	v_add_u32_e32 v2, s68, v1
	ds_read_b128 v[132:135], v2
	ds_read_b128 v[148:151], v2 offset:1024
	ds_read_b128 v[152:155], v2 offset:2048
	ds_read_b128 v[156:159], v2 offset:3072
	v_add_u32_e32 v2, s67, v1
	ds_read_b128 v[160:163], v2
	ds_read_b128 v[164:167], v2 offset:1024
	ds_read_b128 v[168:171], v2 offset:2048
	ds_read_b128 v[172:175], v2 offset:3072
	s_mov_b32 m0, s56
	v_lshl_add_u64 v[232:233], s[34:35], 0, v[138:139]
	ds_read_b128 v[176:179], v146 offset:32768
	ds_read_b128 v[180:183], v146 offset:33792
	ds_read_b128 v[184:187], v146 offset:34816
	ds_read_b128 v[188:191], v146 offset:35840
	ds_read_b128 v[192:195], v146 offset:36864
	ds_read_b128 v[204:207], v146 offset:37888
	ds_read_b128 v[208:211], v146 offset:38912
	ds_read_b128 v[212:215], v146 offset:39936
	global_load_lds_dwordx4 v[232:233], off
	v_lshl_add_u64 v[232:233], s[34:35], 0, v[142:143]
	s_mov_b32 m0, s57
	s_nop 0
	global_load_lds_dwordx4 v[232:233], off
	s_waitcnt vmcnt(8)
	s_waitcnt lgkmcnt(0)
	s_barrier
	s_setprio 1
	s_waitcnt lgkmcnt(0)
	v_mfma_f32_16x16x32_bf16 v[128:131], v[132:135], v[176:179], v[128:131]
	v_mfma_f32_16x16x32_bf16 v[124:127], v[152:155], v[176:179], v[124:127]
	v_mfma_f32_16x16x32_bf16 v[116:119], v[132:135], v[184:187], v[116:119]
	v_mfma_f32_16x16x32_bf16 v[108:111], v[152:155], v[184:187], v[108:111]
	v_mfma_f32_16x16x32_bf16 v[100:103], v[132:135], v[192:195], v[100:103]
	v_mfma_f32_16x16x32_bf16 v[92:95], v[152:155], v[192:195], v[92:95]
	v_mfma_f32_16x16x32_bf16 v[84:87], v[132:135], v[208:211], v[84:87]
	v_mfma_f32_16x16x32_bf16 v[76:79], v[152:155], v[208:211], v[76:79]
	v_mfma_f32_16x16x32_bf16 v[128:131], v[148:151], v[180:183], v[128:131]
	v_mfma_f32_16x16x32_bf16 v[124:127], v[156:159], v[180:183], v[124:127]
	v_mfma_f32_16x16x32_bf16 v[116:119], v[148:151], v[188:191], v[116:119]
	v_mfma_f32_16x16x32_bf16 v[108:111], v[156:159], v[188:191], v[108:111]
	v_mfma_f32_16x16x32_bf16 v[100:103], v[148:151], v[204:207], v[100:103]
	v_mfma_f32_16x16x32_bf16 v[92:95], v[156:159], v[204:207], v[92:95]
	v_mfma_f32_16x16x32_bf16 v[84:87], v[148:151], v[212:215], v[84:87]
	v_mfma_f32_16x16x32_bf16 v[76:79], v[156:159], v[212:215], v[76:79]
	s_setprio 0
	s_setprio 1
	v_mfma_f32_16x16x32_bf16 v[120:123], v[160:163], v[176:179], v[120:123]
	v_mfma_f32_16x16x32_bf16 v[112:115], v[168:171], v[176:179], v[112:115]
	v_mfma_f32_16x16x32_bf16 v[104:107], v[160:163], v[184:187], v[104:107]
	v_mfma_f32_16x16x32_bf16 v[96:99], v[168:171], v[184:187], v[96:99]
	v_mfma_f32_16x16x32_bf16 v[88:91], v[160:163], v[192:195], v[88:91]
	v_mfma_f32_16x16x32_bf16 v[80:83], v[168:171], v[192:195], v[80:83]
	v_mfma_f32_16x16x32_bf16 v[72:75], v[160:163], v[208:211], v[72:75]
	v_mfma_f32_16x16x32_bf16 v[68:71], v[168:171], v[208:211], v[68:71]
	v_mfma_f32_16x16x32_bf16 v[120:123], v[164:167], v[180:183], v[120:123]
	v_mfma_f32_16x16x32_bf16 v[112:115], v[172:175], v[180:183], v[112:115]
	v_mfma_f32_16x16x32_bf16 v[104:107], v[164:167], v[188:191], v[104:107]
	v_mfma_f32_16x16x32_bf16 v[96:99], v[172:175], v[188:191], v[96:99]
	v_mfma_f32_16x16x32_bf16 v[88:91], v[164:167], v[204:207], v[88:91]
	v_mfma_f32_16x16x32_bf16 v[80:83], v[172:175], v[204:207], v[80:83]
	v_mfma_f32_16x16x32_bf16 v[72:75], v[164:167], v[212:215], v[72:75]
	v_mfma_f32_16x16x32_bf16 v[68:71], v[172:175], v[212:215], v[68:71]
	s_setprio 0
	s_barrier
	s_mov_b32 m0, s66
	v_lshl_add_u64 v[144:145], v[144:145], 0, s[94:95]
	ds_read_b128 v[176:179], v146 offset:49152
	ds_read_b128 v[180:183], v146 offset:50176
	ds_read_b128 v[184:187], v146 offset:51200
	ds_read_b128 v[188:191], v146 offset:52224
	ds_read_b128 v[192:195], v146 offset:53248
	ds_read_b128 v[204:207], v146 offset:54272
	ds_read_b128 v[208:211], v146 offset:55296
	ds_read_b128 v[212:215], v146 offset:56320
	global_load_lds_dwordx4 v[144:145], off
	v_lshl_add_u64 v[144:145], v[226:227], 0, s[94:95]
	s_mov_b32 m0, s65
	s_nop 0
	global_load_lds_dwordx4 v[144:145], off
	v_lshl_add_u64 v[144:145], s[30:31], 0, v[136:137]
	s_mov_b32 m0, s75
	s_nop 0
	global_load_lds_dwordx4 v[144:145], off
	v_lshl_add_u64 v[144:145], s[30:31], 0, v[140:141]
	s_mov_b32 m0, s73
	s_nop 0
	global_load_lds_dwordx4 v[144:145], off
	v_lshl_add_u64 v[144:145], v[228:229], 0, s[94:95]
	s_mov_b32 m0, s59
	s_nop 0
	global_load_lds_dwordx4 v[144:145], off
	v_lshl_add_u64 v[144:145], v[230:231], 0, s[94:95]
	s_mov_b32 m0, s60
	s_nop 0
	global_load_lds_dwordx4 v[144:145], off
	s_waitcnt vmcnt(8)
	s_waitcnt lgkmcnt(0)
	s_barrier
	s_setprio 1
	s_waitcnt lgkmcnt(0)
	v_mfma_f32_16x16x32_bf16 v[64:67], v[132:135], v[176:179], v[64:67]
	v_mfma_f32_16x16x32_bf16 v[60:63], v[152:155], v[176:179], v[60:63]
	v_mfma_f32_16x16x32_bf16 v[52:55], v[132:135], v[184:187], v[52:55]
	v_mfma_f32_16x16x32_bf16 v[44:47], v[152:155], v[184:187], v[44:47]
	v_mfma_f32_16x16x32_bf16 v[36:39], v[132:135], v[192:195], v[36:39]
	v_mfma_f32_16x16x32_bf16 v[28:31], v[152:155], v[192:195], v[28:31]
	v_mfma_f32_16x16x32_bf16 v[20:23], v[132:135], v[208:211], v[20:23]
	v_mfma_f32_16x16x32_bf16 v[12:15], v[152:155], v[208:211], v[12:15]
	v_mfma_f32_16x16x32_bf16 v[64:67], v[148:151], v[180:183], v[64:67]
	v_mfma_f32_16x16x32_bf16 v[60:63], v[156:159], v[180:183], v[60:63]
	v_mfma_f32_16x16x32_bf16 v[52:55], v[148:151], v[188:191], v[52:55]
	v_mfma_f32_16x16x32_bf16 v[44:47], v[156:159], v[188:191], v[44:47]
	v_mfma_f32_16x16x32_bf16 v[36:39], v[148:151], v[204:207], v[36:39]
	v_mfma_f32_16x16x32_bf16 v[28:31], v[156:159], v[204:207], v[28:31]
	v_mfma_f32_16x16x32_bf16 v[20:23], v[148:151], v[212:215], v[20:23]
	v_mfma_f32_16x16x32_bf16 v[12:15], v[156:159], v[212:215], v[12:15]
	s_setprio 0
	s_setprio 1
	v_mfma_f32_16x16x32_bf16 v[56:59], v[160:163], v[176:179], v[56:59]
	v_mfma_f32_16x16x32_bf16 v[48:51], v[168:171], v[176:179], v[48:51]
	v_mfma_f32_16x16x32_bf16 v[40:43], v[160:163], v[184:187], v[40:43]
	v_mfma_f32_16x16x32_bf16 v[32:35], v[168:171], v[184:187], v[32:35]
	v_mfma_f32_16x16x32_bf16 v[24:27], v[160:163], v[192:195], v[24:27]
	v_mfma_f32_16x16x32_bf16 v[16:19], v[168:171], v[192:195], v[16:19]
	v_mfma_f32_16x16x32_bf16 v[8:11], v[160:163], v[208:211], v[8:11]
	v_mfma_f32_16x16x32_bf16 v[4:7], v[168:171], v[208:211], v[4:7]
	v_mfma_f32_16x16x32_bf16 v[56:59], v[164:167], v[180:183], v[56:59]
	v_mfma_f32_16x16x32_bf16 v[48:51], v[172:175], v[180:183], v[48:51]
	v_mfma_f32_16x16x32_bf16 v[40:43], v[164:167], v[188:191], v[40:43]
	v_mfma_f32_16x16x32_bf16 v[32:35], v[172:175], v[188:191], v[32:35]
	v_mfma_f32_16x16x32_bf16 v[24:27], v[164:167], v[204:207], v[24:27]
	v_mfma_f32_16x16x32_bf16 v[16:19], v[172:175], v[204:207], v[16:19]
	v_mfma_f32_16x16x32_bf16 v[8:11], v[164:167], v[212:215], v[8:11]
	v_mfma_f32_16x16x32_bf16 v[4:7], v[172:175], v[212:215], v[4:7]
	s_setprio 0
	s_mov_b64 s[36:37], 0
	s_mov_b64 s[30:31], -1
	s_mov_b64 s[34:35], 0x100
	s_barrier
	s_cbranch_vccz .LBB0_2674
	s_and_b64 vcc, exec, s[12:13]
	s_cbranch_vccz .LBB0_2677
	s_barrier
